# v043 + ret_r3 GroupNorm 8-lane sums: ds_bpermute xor 1/2/4 shuffles -> v_add_f32_dpp (quad_perm, quad_perm, row_half_mirror)
# speedup vs baseline: 1.0029x; 1.0029x over previous
; #define LAS __attribute__((address_space(3)))
; __device__ __forceinline__ void rot8r(const u32x4 x1, const u32x4 x2, const RetPref& p, float scale, float (&o1)[8], float (&o2)[8]) {
;     const float cs[8] = {p.c0.x, p.c0.y, p.c0.z, p.c0.w, p.c1.x, p.c1.y, p.c1.z, p.c1.w}, sn[8] = {p.s0.x, p.s0.y, p.s0.z, p.s0.w, p.s1.x, p.s1.y, p.s1.z, p.s1.w};
;     const unsigned w1[4] = {x1.x, x1.y, x1.z, x1.w}, w2[4] = {x2.x, x2.y, x2.z, x2.w};
; #pragma unroll
;     for (int j = 0; j < 8; ++j) {
;         const float a = (j & 1) ? bfhi(w1[j >> 1]) : bflo(w1[j >> 1]);
;         const float bb = (j & 1) ? bfhi(w2[j >> 1]) : bflo(w2[j >> 1]);
;         o1[j] = (a * cs[j] - bb * sn[j]) * scale;
;         o2[j] = (bb * cs[j] + a * sn[j]) * scale;
;     }
; }
; __device__ __forceinline__ bf16x8 trb_frag(const LAS unsigned char* tile, unsigned lane, unsigned c, unsigned ks) {
;     const v4i16_t lo = __builtin_amdgcn_ds_read_tr16_b64_v4i16((LAS v4i16_t*)(tile + trb_addr16(lane, c, ks, 0)));
;     const v4i16_t hi = __builtin_amdgcn_ds_read_tr16_b64_v4i16((LAS v4i16_t*)(tile + trb_addr16(lane, c, ks, 1)));
;     return (bf16x8){lo[0], lo[1], lo[2], lo[3], hi[0], hi[1], hi[2], hi[3]};
; }
; __device__ __forceinline__ void ret_r3_phase(LAS unsigned char* lds, const bf16_t* proj, const float* cosT, const float* sinT, const float* gst, bf16_t* ycat, int G, int b) {
;     ...
;             const u32x4 gc0 = pn.g0, gc1 = pn.g1;
;             {
;                 float o1[8], o2[8];
;                 rot8r(pn.q1, pn.q2, pn, 0.08838834764831845f, o1, o2);
;                 *(LAS u32x4*)(QS + m * 136 + tq * 8) = (u32x4){pk2(o1[0], o1[1]), pk2(o1[2], o1[3]), pk2(o1[4], o1[5]), pk2(o1[6], o1[7])};
;                 *(LAS u32x4*)(QS + m * 136 + 64 + tq * 8) = (u32x4){pk2(o2[0], o2[1]), pk2(o2[2], o2[3]), pk2(o2[4], o2[5]), pk2(o2[6], o2[7])};
;                 ret_stage_kv(pn, KT, VT, m, tq, kdec, o1, o2);
;                 *(LAS u32x4*)(KS + m * 136 + tq * 8) = (u32x4){pk2(o1[0], o1[1]), pk2(o1[2], o1[3]), pk2(o1[4], o1[5]), pk2(o1[6], o1[7])};
;                 *(LAS u32x4*)(KS + m * 136 + 64 + tq * 8) = (u32x4){pk2(o2[0], o2[1]), pk2(o2[2], o2[3]), pk2(o2[4], o2[5]), pk2(o2[6], o2[7])};
;             }
;             if (i + 1 < 8) ret_prefetch<true>(pn, proj, cosT, sinT, s + 64, h, tq);
;             __syncthreads();
.LBB0_405:
	s_waitcnt vmcnt(4)
	v_lshlrev_b32_e32 v2, 16, v78
	v_and_b32_e32 v3, 0xffff0000, v78
	v_lshlrev_b32_e32 v4, 16, v74
	v_and_b32_e32 v5, 0xffff0000, v74
	v_pk_mul_f32 v[22:23], v[66:67], v[2:3]
	v_add_u32_e32 v144, s44, v222
	s_waitcnt vmcnt(3)
	v_pk_fma_f32 v[22:23], v[70:71], v[4:5], v[22:23] neg_lo:[0,0,1] neg_hi:[0,0,1]
	v_pk_mul_f32 v[4:5], v[66:67], v[4:5]
	v_pk_mul_f32 v[22:23], v[22:23], s[54:55] op_sel_hi:[1,0]
	v_pk_fma_f32 v[2:3], v[70:71], v[2:3], v[4:5]
	v_lshlrev_b32_e32 v4, 16, v75
	v_pk_mul_f32 v[24:25], v[2:3], s[54:55] op_sel_hi:[1,0]
	v_lshlrev_b32_e32 v2, 16, v79
	v_and_b32_e32 v3, 0xffff0000, v79
	v_and_b32_e32 v5, 0xffff0000, v75
	v_pk_mul_f32 v[74:75], v[68:69], v[2:3]
	v_add_u32_e32 v223, 0x400, v199
	v_pk_fma_f32 v[74:75], v[72:73], v[4:5], v[74:75] neg_lo:[0,0,1] neg_hi:[0,0,1]
	v_pk_mul_f32 v[4:5], v[68:69], v[4:5]
	v_pk_mul_f32 v[74:75], v[74:75], s[54:55] op_sel_hi:[1,0]
	v_pk_fma_f32 v[2:3], v[72:73], v[2:3], v[4:5]
	v_lshlrev_b32_e32 v4, 16, v76
	v_pk_mul_f32 v[78:79], v[2:3], s[54:55] op_sel_hi:[1,0]
	v_lshlrev_b32_e32 v2, 16, v80
	v_and_b32_e32 v3, 0xffff0000, v80
	v_and_b32_e32 v5, 0xffff0000, v76
	s_waitcnt vmcnt(1)
	v_pk_mul_f32 v[90:91], v[62:63], v[2:3]
	v_mov_b32_e32 v141, v140
	v_pk_fma_f32 v[90:91], v[50:51], v[4:5], v[90:91] neg_lo:[0,0,1] neg_hi:[0,0,1]
	v_pk_mul_f32 v[4:5], v[62:63], v[4:5]
	v_pk_mul_f32 v[90:91], v[90:91], s[54:55] op_sel_hi:[1,0]
	v_pk_fma_f32 v[2:3], v[50:51], v[2:3], v[4:5]
	v_lshlrev_b32_e32 v4, 16, v77
	v_pk_mul_f32 v[92:93], v[2:3], s[54:55] op_sel_hi:[1,0]
	v_lshlrev_b32_e32 v2, 16, v81
	v_and_b32_e32 v3, 0xffff0000, v81
	v_and_b32_e32 v5, 0xffff0000, v77
	v_pk_mul_f32 v[76:77], v[64:65], v[2:3]
	s_add_i32 s44, s44, 64
	v_pk_fma_f32 v[76:77], v[52:53], v[4:5], v[76:77] neg_lo:[0,0,1] neg_hi:[0,0,1]
	v_pk_mul_f32 v[4:5], v[64:65], v[4:5]
	v_pk_mul_f32 v[76:77], v[76:77], s[54:55] op_sel_hi:[1,0]
	v_pk_fma_f32 v[2:3], v[52:53], v[2:3], v[4:5]
	v_cvt_pk_bf16_f32 v4, v90, v91
	v_pk_mul_f32 v[80:81], v[2:3], s[54:55] op_sel_hi:[1,0]
	v_cvt_pk_bf16_f32 v2, v22, v23
	v_cvt_pk_bf16_f32 v3, v74, v75
	v_cvt_pk_bf16_f32 v5, v76, v77
	ds_write_b128 v147, v[2:5]
	v_cvt_pk_bf16_f32 v2, v24, v25
	v_cvt_pk_bf16_f32 v3, v78, v79
	v_cvt_pk_bf16_f32 v4, v92, v93
	v_cvt_pk_bf16_f32 v5, v80, v81
	v_lshlrev_b32_e32 v22, 16, v58
	v_and_b32_e32 v23, 0xffff0000, v58
	v_lshlrev_b32_e32 v58, 16, v59
	v_and_b32_e32 v59, 0xffff0000, v59
	ds_write_b128 v147, v[2:5] offset:128
	v_lshlrev_b32_e32 v24, 16, v54
	v_and_b32_e32 v25, 0xffff0000, v54
	v_pk_mul_f32 v[2:3], v[66:67], v[22:23]
	v_lshlrev_b32_e32 v54, 16, v55
	v_and_b32_e32 v55, 0xffff0000, v55
	v_pk_mul_f32 v[4:5], v[68:69], v[58:59]
	v_pk_fma_f32 v[74:75], v[70:71], v[24:25], v[2:3] neg_lo:[0,0,1] neg_hi:[0,0,1]
	v_pk_fma_f32 v[76:77], v[72:73], v[54:55], v[4:5] neg_lo:[0,0,1] neg_hi:[0,0,1]
	v_pk_mul_f32 v[2:3], v[138:139], v[74:75]
	v_pk_mul_f32 v[4:5], v[138:139], v[76:77]
	v_lshlrev_b32_e32 v78, 16, v60
	v_and_b32_e32 v79, 0xffff0000, v60
	v_lshlrev_b32_e32 v60, 16, v61
	v_and_b32_e32 v61, 0xffff0000, v61
	v_cvt_pk_bf16_f32 v2, v2, v3
	v_cvt_pk_bf16_f32 v3, v4, v5
	v_lshlrev_b32_e32 v80, 16, v56
	v_and_b32_e32 v81, 0xffff0000, v56
	v_pk_mul_f32 v[4:5], v[62:63], v[78:79]
	v_lshlrev_b32_e32 v56, 16, v57
	v_and_b32_e32 v57, 0xffff0000, v57
	v_pk_mul_f32 v[92:93], v[64:65], v[60:61]
	v_pk_fma_f32 v[90:91], v[50:51], v[80:81], v[4:5] neg_lo:[0,0,1] neg_hi:[0,0,1]
	v_pk_fma_f32 v[92:93], v[52:53], v[56:57], v[92:93] neg_lo:[0,0,1] neg_hi:[0,0,1]
	v_pk_mul_f32 v[4:5], v[138:139], v[90:91]
	v_pk_mul_f32 v[94:95], v[138:139], v[92:93]
	v_cvt_pk_bf16_f32 v4, v4, v5
	v_cvt_pk_bf16_f32 v5, v94, v95
	ds_write_b128 v189, v[2:5] offset:34816
	v_pk_mul_f32 v[2:3], v[66:67], v[24:25]
	v_pk_mul_f32 v[4:5], v[68:69], v[54:55]
	v_pk_fma_f32 v[22:23], v[70:71], v[22:23], v[2:3]
	v_pk_fma_f32 v[24:25], v[72:73], v[58:59], v[4:5]
	v_pk_mul_f32 v[2:3], v[138:139], v[22:23]
	v_pk_mul_f32 v[4:5], v[138:139], v[24:25]
	v_cvt_pk_bf16_f32 v2, v2, v3
	v_cvt_pk_bf16_f32 v3, v4, v5
	v_pk_mul_f32 v[4:5], v[62:63], v[80:81]
	v_pk_mul_f32 v[54:55], v[64:65], v[56:57]
	v_pk_fma_f32 v[50:51], v[50:51], v[78:79], v[4:5]
	v_pk_fma_f32 v[52:53], v[52:53], v[60:61], v[54:55]
	v_pk_mul_f32 v[4:5], v[138:139], v[50:51]
	v_pk_mul_f32 v[54:55], v[138:139], v[52:53]
	v_cvt_pk_bf16_f32 v4, v4, v5
	v_cvt_pk_bf16_f32 v5, v54, v55
	ds_write_b128 v189, v[2:5] offset:35840
	ds_write_b128 v190, v[46:49] offset:53248
	ds_write_b128 v191, v[42:45] offset:53248
	v_cvt_pk_bf16_f32 v2, v74, v75
	v_cvt_pk_bf16_f32 v3, v76, v77
	v_cvt_pk_bf16_f32 v4, v90, v91
	v_cvt_pk_bf16_f32 v5, v92, v93
	ds_write_b128 v147, v[2:5] offset:17408
	v_cvt_pk_bf16_f32 v2, v22, v23
	v_cvt_pk_bf16_f32 v3, v24, v25
	v_cvt_pk_bf16_f32 v4, v50, v51
	v_cvt_pk_bf16_f32 v5, v52, v53
	ds_write_b128 v147, v[2:5] offset:17536
	v_add_u32_e32 v2, 64, v144
	v_mov_b64_e32 v[4:5], s[66:67]
	v_mad_i64_i32 v[4:5], s[0:1], v2, s5, v[4:5]
	v_lshl_add_u64 v[22:23], v[4:5], 0, v[106:107]
	v_lshl_add_u64 v[4:5], v[4:5], 0, v[118:119]
	v_ashrrev_i32_e32 v3, 31, v2
	v_add_co_u32_e32 v90, vcc, s4, v4
	v_lshl_add_u64 v[24:25], v[4:5], 0, s[46:47]
	s_nop 0
	v_addc_co_u32_e32 v91, vcc, 0, v5, vcc
	v_lshlrev_b64 v[2:3], 8, v[2:3]
	global_load_dwordx4 v[54:57], v[22:23], off offset:2048
	global_load_dwordx4 v[58:61], v[22:23], off offset:2176
	global_load_dwordx4 v[46:49], v[90:91], off
	global_load_dwordx4 v[42:45], v[24:25], off offset:16
	v_lshl_add_u64 v[24:25], v[112:113], 0, v[2:3]
	v_lshl_add_u64 v[2:3], v[114:115], 0, v[2:3]
	global_load_dwordx4 v[50:53], v[24:25], off offset:16
	global_load_dwordx4 v[70:73], v[24:25], off
	global_load_dwordx4 v[62:65], v[2:3], off offset:16
	global_load_dwordx4 v[66:69], v[2:3], off
	global_load_dwordx4 v[74:77], v[22:23], off
	global_load_dwordx4 v[78:81], v[22:23], off offset:128
	v_lshl_add_u64 v[2:3], v[4:5], 0, s[48:49]
	global_load_dwordx4 v[22:25], v[90:91], off offset:2048
	s_nop 0
	global_load_dwordx4 v[2:5], v[2:3], off offset:16
	s_waitcnt lgkmcnt(0)
	s_barrier
; #define LAS __attribute__((address_space(3)))
; __device__ __forceinline__ unsigned f2bf(float f) { return pk2(f, 0.f) & 0xffffu; }
; __device__ __forceinline__ void ret_r3_phase(LAS unsigned char* lds, const bf16_t* proj, const float* cosT, const float* sinT, const float* gst, bf16_t* ycat, int G, int b) {
;     ...
;             {
;                 const int ct = wid & 3, mt0 = (wid >> 2) * 2;
;                 f32x4 sacc[2] = {(f32x4){0.f, 0.f, 0.f, 0.f}, (f32x4){0.f, 0.f, 0.f, 0.f}};
; #pragma unroll
;                 for (int ks = 0; ks < 4; ++ks) {
;                     const bf16x8 a = *(const LAS bf16x8*)(QS + (ct * 16 + fr) * 136 + ks * 32 + fq * 8);
; #pragma unroll
;                     for (int j = 0; j < 2; ++j) { const bf16x8 bb = *(const LAS bf16x8*)(KS + ((mt0 + j) * 16 + fr) * 136 + ks * 32 + fq * 8); sacc[j] = mfma16(a, bb, sacc[j]); }
;                 }
; #pragma unroll
;                 for (int j = 0; j < 2; ++j)
; #pragma unroll
;                     for (int r = 0; r < 4; ++r) { const int c = ct * 16 + fq * 4 + r, mm = (mt0 + j) * 16 + fr;
;                         PS[c * 72 + mm] = (bf16_t)f2bf(sacc[j][r] * pdec[j][r]); }
;                 asm volatile("" ::: "memory");
; #pragma unroll
;                 for (int c4 = 0; c4 < 4; ++c4) oacc[c4] = (f32x4){0.f, 0.f, 0.f, 0.f};
; #pragma unroll
;                 for (int a4 = 0; a4 < 4; ++a4) {
;                     u32x4 bw; bw.x = pk2(S[2 * a4][0], S[2 * a4][1]); bw.y = pk2(S[2 * a4][2], S[2 * a4][3]); bw.z = pk2(S[2 * a4 + 1][0], S[2 * a4 + 1][1]); bw.w = pk2(S[2 * a4 + 1][2], S[2 * a4 + 1][3]);
;                     const bf16x8 bb = __builtin_bit_cast(bf16x8, bw);
; #pragma unroll
;                     for (int c4 = 0; c4 < 4; ++c4) {
;                         const u32x2 lo = *(const LAS u32x2*)(QS + (c4 * 16 + fr) * 136 + a4 * 32 + fq * 4), hi = *(const LAS u32x2*)(QS + (c4 * 16 + fr) * 136 + a4 * 32 + 16 + fq * 4);
;                         const bf16x8 a = __builtin_bit_cast(bf16x8, (u32x4){lo.x, lo.y, hi.x, hi.y});
;                         oacc[c4] = mfma16(a, bb, oacc[c4]);
;                     }
;                     asm volatile("" ::: "memory");
;                 }
; #pragma unroll
;                 for (int c4 = 0; c4 < 4; ++c4)
; #pragma unroll
;                     for (int r = 0; r < 4; ++r) oacc[c4][r] *= odec[c4][r];
	ds_read_b128 v[90:93], v148
	ds_read_b128 v[94:97], v192 offset:17408
	ds_read_b128 v[98:101], v193 offset:17408
	s_waitcnt lgkmcnt(1)
	v_mfma_f32_16x16x32_bf16 v[94:97], v[90:93], v[94:97], 0
	s_cmpk_eq_i32 s44, 0x1c0
	s_waitcnt lgkmcnt(0)
	v_mfma_f32_16x16x32_bf16 v[90:93], v[90:93], v[98:101], 0
	ds_read_b128 v[98:101], v148 offset:64
	ds_read_b128 v[102:105], v192 offset:17472
	s_waitcnt lgkmcnt(0)
	v_mfma_f32_16x16x32_bf16 v[94:97], v[98:101], v[102:105], v[94:97]
	ds_read_b128 v[102:105], v193 offset:17472
	s_waitcnt lgkmcnt(0)
	v_mfma_f32_16x16x32_bf16 v[90:93], v[98:101], v[102:105], v[90:93]
	ds_read_b128 v[98:101], v148 offset:128
	ds_read_b128 v[102:105], v192 offset:17536
	s_waitcnt lgkmcnt(0)
	v_mfma_f32_16x16x32_bf16 v[94:97], v[98:101], v[102:105], v[94:97]
	ds_read_b128 v[102:105], v193 offset:17536
	s_waitcnt lgkmcnt(0)
	v_mfma_f32_16x16x32_bf16 v[90:93], v[98:101], v[102:105], v[90:93]
	ds_read_b128 v[98:101], v148 offset:192
	ds_read_b128 v[102:105], v192 offset:17600
	s_waitcnt lgkmcnt(0)
	v_mfma_f32_16x16x32_bf16 v[94:97], v[98:101], v[102:105], v[94:97]
	ds_read_b128 v[102:105], v193 offset:17600
	s_waitcnt lgkmcnt(0)
	v_mfma_f32_16x16x32_bf16 v[90:93], v[98:101], v[102:105], v[90:93]
	s_nop 4
	v_mul_f32_e32 v94, v214, v94
	v_cvt_pk_bf16_f32 v94, v94, s0
	ds_write_b16 v194, v94
	v_mul_f32_e32 v94, v215, v95
	v_cvt_pk_bf16_f32 v94, v94, s0
	ds_write_b16 v194, v94 offset:144
	v_mul_f32_e32 v94, v216, v96
	v_mul_f32_e32 v90, v218, v90
	v_cvt_pk_bf16_f32 v94, v94, s0
	v_cvt_pk_bf16_f32 v90, v90, s0
	ds_write_b16 v194, v94 offset:288
	v_mul_f32_e32 v94, v217, v97
	ds_write_b16 v195, v90
	v_mul_f32_e32 v90, v219, v91
	v_cvt_pk_bf16_f32 v94, v94, s0
	v_cvt_pk_bf16_f32 v90, v90, s0
	ds_write_b16 v194, v94 offset:432
	ds_write_b16 v195, v90 offset:144
	v_mul_f32_e32 v90, v220, v92
	v_cvt_pk_bf16_f32 v90, v90, s0
	ds_write_b16 v195, v90 offset:288
	v_mul_f32_e32 v90, v221, v93
	v_cvt_pk_bf16_f32 v90, v90, s0
	ds_write_b16 v195, v90 offset:432
	ds_read2_b64 v[94:97], v177 offset1:4
	ds_read2_b64 v[98:101], v178 offset1:4
	ds_read2_b64 v[102:105], v179 offset1:4
	ds_read2_b64 v[224:227], v180 offset1:4
	ds_read2_b64 v[228:231], v177 offset0:8 offset1:12
	v_cvt_pk_bf16_f32 v90, v38, v39
	v_cvt_pk_bf16_f32 v91, v40, v41
	v_cvt_pk_bf16_f32 v92, v34, v35
	v_cvt_pk_bf16_f32 v93, v36, v37
	v_pk_mul_f32 v[40:41], v[140:141], v[40:41]
	v_pk_mul_f32 v[38:39], v[142:143], v[38:39]
	s_waitcnt lgkmcnt(4)
	v_mfma_f32_16x16x32_bf16 v[94:97], v[94:97], v[90:93], 0
	v_mul_f32_e64 v36, v140, v36
	v_mul_f32_e64 v37, v141, v37
	v_pk_mul_f32 v[34:35], v[142:143], v[34:35]
	s_waitcnt lgkmcnt(3)
	v_mfma_f32_16x16x32_bf16 v[98:101], v[98:101], v[90:93], 0
	s_waitcnt lgkmcnt(2)
	v_mfma_f32_16x16x32_bf16 v[102:105], v[102:105], v[90:93], 0
	s_waitcnt lgkmcnt(1)
	v_mfma_f32_16x16x32_bf16 v[90:93], v[224:227], v[90:93], 0
	v_cvt_pk_bf16_f32 v224, v30, v31
	v_cvt_pk_bf16_f32 v225, v32, v33
	v_cvt_pk_bf16_f32 v226, v26, v27
	v_cvt_pk_bf16_f32 v227, v28, v29
	v_pk_mul_f32 v[32:33], v[140:141], v[32:33]
	v_pk_mul_f32 v[30:31], v[142:143], v[30:31]
	s_waitcnt lgkmcnt(0)
	v_mfma_f32_16x16x32_bf16 v[94:97], v[228:231], v[224:227], v[94:97]
	ds_read2_b64 v[228:231], v178 offset0:8 offset1:12
	v_pk_mul_f32 v[28:29], v[140:141], v[28:29]
	v_pk_mul_f32 v[26:27], v[142:143], v[26:27]
	s_waitcnt lgkmcnt(0)
	v_mfma_f32_16x16x32_bf16 v[98:101], v[228:231], v[224:227], v[98:101]
	ds_read2_b64 v[228:231], v179 offset0:8 offset1:12
	s_waitcnt lgkmcnt(0)
	v_mfma_f32_16x16x32_bf16 v[102:105], v[228:231], v[224:227], v[102:105]
	ds_read2_b64 v[228:231], v180 offset0:8 offset1:12
	s_waitcnt lgkmcnt(0)
	v_mfma_f32_16x16x32_bf16 v[90:93], v[228:231], v[224:227], v[90:93]
	ds_read2_b64 v[228:231], v177 offset0:16 offset1:20
	v_cvt_pk_bf16_f32 v224, v18, v19
	v_cvt_pk_bf16_f32 v225, v20, v21
	v_cvt_pk_bf16_f32 v226, v14, v15
	v_cvt_pk_bf16_f32 v227, v16, v17
	v_pk_mul_f32 v[20:21], v[140:141], v[20:21]
	v_pk_mul_f32 v[18:19], v[142:143], v[18:19]
	s_waitcnt lgkmcnt(0)
	v_mfma_f32_16x16x32_bf16 v[94:97], v[228:231], v[224:227], v[94:97]
	ds_read2_b64 v[228:231], v178 offset0:16 offset1:20
	v_pk_mul_f32 v[16:17], v[140:141], v[16:17]
	v_pk_mul_f32 v[14:15], v[142:143], v[14:15]
	s_waitcnt lgkmcnt(0)
	v_mfma_f32_16x16x32_bf16 v[98:101], v[228:231], v[224:227], v[98:101]
	ds_read2_b64 v[228:231], v179 offset0:16 offset1:20
	s_waitcnt lgkmcnt(0)
	v_mfma_f32_16x16x32_bf16 v[102:105], v[228:231], v[224:227], v[102:105]
	ds_read2_b64 v[228:231], v180 offset0:16 offset1:20
	s_waitcnt lgkmcnt(0)
	v_mfma_f32_16x16x32_bf16 v[90:93], v[228:231], v[224:227], v[90:93]
	ds_read2_b64 v[228:231], v177 offset0:24 offset1:28
	v_cvt_pk_bf16_f32 v224, v10, v11
	v_cvt_pk_bf16_f32 v225, v12, v13
	v_cvt_pk_bf16_f32 v226, v6, v7
	v_cvt_pk_bf16_f32 v227, v8, v9
	v_pk_mul_f32 v[12:13], v[140:141], v[12:13]
	v_pk_mul_f32 v[10:11], v[142:143], v[10:11]
	s_waitcnt lgkmcnt(0)
	v_mfma_f32_16x16x32_bf16 v[94:97], v[228:231], v[224:227], v[94:97]
	ds_read2_b64 v[228:231], v178 offset0:24 offset1:28
	v_pk_mul_f32 v[8:9], v[140:141], v[8:9]
	v_pk_mul_f32 v[6:7], v[142:143], v[6:7]
	s_waitcnt lgkmcnt(0)
	v_mfma_f32_16x16x32_bf16 v[98:101], v[228:231], v[224:227], v[98:101]
	ds_read2_b64 v[228:231], v179 offset0:24 offset1:28
	s_nop 1
	v_pk_mul_f32 v[96:97], v[124:125], v[96:97]
	v_pk_mul_f32 v[94:95], v[122:123], v[94:95]
	s_waitcnt lgkmcnt(0)
	v_mfma_f32_16x16x32_bf16 v[102:105], v[228:231], v[224:227], v[102:105]
	ds_read2_b64 v[228:231], v180 offset0:24 offset1:28
	s_waitcnt lgkmcnt(0)
	v_mfma_f32_16x16x32_bf16 v[90:93], v[228:231], v[224:227], v[90:93]
	s_barrier
; #define LAS __attribute__((address_space(3)))
; __device__ __forceinline__ f32x4 mfma16(bf16x8 a, bf16x8 b, f32x4 c) { return __builtin_amdgcn_mfma_f32_16x16x32_bf16(a, b, c, 0, 0, 0); }
; __device__ __forceinline__ void ret_state_update(f32x4 (&S)[8], const LAS bf16_t* KT, const LAS bf16_t* VT, float dec, int wid, int fr, int fq) {
;     ...
; #pragma unroll
;     for (int ks = 0; ks < 2; ++ks) {
;         const bf16x8 bb = trb_frag((const LAS unsigned char*)VT, lane, wid, ks);
; #pragma unroll
;         for (int tt = 0; tt < 8; ++tt) { const bf16x8 a = trb_frag((const LAS unsigned char*)KT, lane, tt, ks); S[tt] = mfma16(a, bb, S[tt]); }
;     }
; __device__ __forceinline__ void ret_r3_phase(LAS unsigned char* lds, const bf16_t* proj, const float* cosT, const float* sinT, const float* gst, bf16_t* ycat, int G, int b) {
;     ...
;             {
; #pragma unroll
;                 for (int ks = 0; ks < 2; ++ks) {
;                     const bf16x8 bb = trb_frag((const LAS unsigned char*)VT, (unsigned)lane, wid, ks);
; #pragma unroll
;                     for (int c4 = 0; c4 < 4; ++c4) { const bf16x8 a = *(const LAS bf16x8*)(PS + (c4 * 16 + fr) * 72 + ks * 32 + fq * 8); oacc[c4] = mfma16(a, bb, oacc[c4]); }
;                 }
; #pragma unroll
;                 for (int c4 = 0; c4 < 4; ++c4)
; #pragma unroll
;                     for (int r = 0; r < 4; ++r) OS[(c4 * 16 + fq * 4 + r) * 132 + wid * 16 + fr] = oacc[c4][r];
;                 ret_state_update(S, KT, VT, dec, wid, fr, fq);
;             }
	ds_read_b64_tr_b16 v[224:225], v196 offset:53248
	ds_read_b64_tr_b16 v[226:227], v197 offset:53504
	ds_read_b128 v[228:231], v198
	s_waitcnt lgkmcnt(0)
	v_mfma_f32_16x16x32_bf16 v[94:97], v[228:231], v[224:227], v[94:97]
	ds_read_b128 v[228:231], v198 offset:2304
	v_pk_mul_f32 v[100:101], v[128:129], v[100:101]
	v_pk_mul_f32 v[98:99], v[126:127], v[98:99]
	v_pk_mul_f32 v[104:105], v[132:133], v[104:105]
	v_pk_mul_f32 v[102:103], v[130:131], v[102:103]
	s_waitcnt lgkmcnt(0)
	v_mfma_f32_16x16x32_bf16 v[98:101], v[228:231], v[224:227], v[98:101]
	ds_read_b128 v[228:231], v198 offset:4608
	v_pk_mul_f32 v[92:93], v[136:137], v[92:93]
	v_pk_mul_f32 v[90:91], v[134:135], v[90:91]
	s_waitcnt lgkmcnt(0)
	v_mfma_f32_16x16x32_bf16 v[102:105], v[228:231], v[224:227], v[102:105]
	ds_read_b128 v[228:231], v198 offset:6912
	s_waitcnt lgkmcnt(0)
	v_mfma_f32_16x16x32_bf16 v[90:93], v[228:231], v[224:227], v[90:93]
	ds_read_b64_tr_b16 v[224:225], v196 offset:61440
	ds_read_b64_tr_b16 v[226:227], v197 offset:61696
	ds_read_b128 v[228:231], v198 offset:64
	s_waitcnt lgkmcnt(0)
	v_mfma_f32_16x16x32_bf16 v[228:231], v[228:231], v[224:227], v[94:97]
	s_nop 2
	ds_read_b128 v[94:97], v198 offset:2368
	s_waitcnt lgkmcnt(0)
	v_mfma_f32_16x16x32_bf16 v[98:101], v[94:97], v[224:227], v[98:101]
	ds_read_b128 v[94:97], v198 offset:4672
	s_waitcnt lgkmcnt(0)
	v_mfma_f32_16x16x32_bf16 v[94:97], v[94:97], v[224:227], v[102:105]
	s_nop 2
	ds_read_b128 v[102:105], v198 offset:6976
	ds_write2_b32 v199, v228, v229 offset1:132
	v_add_u32_e32 v228, 0x6200, v199
	s_waitcnt lgkmcnt(1)
	v_mfma_f32_16x16x32_bf16 v[90:93], v[102:105], v[224:227], v[90:93]
	v_add_u32_e32 v224, 0x2000, v199
	v_add_u32_e32 v225, 0x2400, v199
	v_add_u32_e32 v226, 0x4200, v199
	v_add_u32_e32 v227, 0x4600, v199
	v_add_u32_e32 v229, 0x6600, v199
	ds_write2_b32 v223, v230, v231 offset0:8 offset1:140
	ds_write2_b32 v224, v98, v99 offset0:64 offset1:196
	ds_write2_b32 v225, v100, v101 offset0:72 offset1:204
	ds_write2_b32 v226, v94, v95 offset1:132
	ds_write2_b32 v227, v96, v97 offset0:8 offset1:140
	ds_write2_b32 v228, v90, v91 offset0:64 offset1:196
	ds_write2_b32 v229, v92, v93 offset0:72 offset1:204
	ds_read_b64_tr_b16 v[90:91], v196 offset:53248
	ds_read_b64_tr_b16 v[92:93], v197 offset:53504
	ds_read_b64_tr_b16 v[94:95], v181 offset:34816
	ds_read_b64_tr_b16 v[96:97], v182 offset:35072
	s_waitcnt lgkmcnt(0)
	v_mfma_f32_16x16x32_bf16 v[38:41], v[94:97], v[90:93], v[38:41]
	ds_read_b64_tr_b16 v[94:95], v183 offset:34816
	ds_read_b64_tr_b16 v[96:97], v184 offset:35072
	s_waitcnt lgkmcnt(0)
	v_mfma_f32_16x16x32_bf16 v[34:37], v[94:97], v[90:93], v[34:37]
	ds_read_b64_tr_b16 v[94:95], v181 offset:35328
	ds_read_b64_tr_b16 v[96:97], v182 offset:35584
	s_waitcnt lgkmcnt(0)
	v_mfma_f32_16x16x32_bf16 v[30:33], v[94:97], v[90:93], v[30:33]
	ds_read_b64_tr_b16 v[94:95], v183 offset:35328
	ds_read_b64_tr_b16 v[96:97], v184 offset:35584
	s_waitcnt lgkmcnt(0)
	v_mfma_f32_16x16x32_bf16 v[26:29], v[94:97], v[90:93], v[26:29]
	ds_read_b64_tr_b16 v[94:95], v181 offset:35840
	ds_read_b64_tr_b16 v[96:97], v182 offset:36096
	s_waitcnt lgkmcnt(0)
	v_mfma_f32_16x16x32_bf16 v[18:21], v[94:97], v[90:93], v[18:21]
	ds_read_b64_tr_b16 v[94:95], v183 offset:35840
	ds_read_b64_tr_b16 v[96:97], v184 offset:36096
	s_waitcnt lgkmcnt(0)
	v_mfma_f32_16x16x32_bf16 v[14:17], v[94:97], v[90:93], v[14:17]
	ds_read_b64_tr_b16 v[94:95], v181 offset:36352
	ds_read_b64_tr_b16 v[96:97], v182 offset:36608
	s_waitcnt lgkmcnt(0)
	v_mfma_f32_16x16x32_bf16 v[10:13], v[94:97], v[90:93], v[10:13]
	ds_read_b64_tr_b16 v[94:95], v183 offset:36352
	ds_read_b64_tr_b16 v[96:97], v184 offset:36608
	s_waitcnt lgkmcnt(0)
	v_mfma_f32_16x16x32_bf16 v[6:9], v[94:97], v[90:93], v[6:9]
	ds_read_b64_tr_b16 v[90:91], v196 offset:61440
	ds_read_b64_tr_b16 v[92:93], v197 offset:61696
	ds_read_b64_tr_b16 v[94:95], v181 offset:43008
	ds_read_b64_tr_b16 v[96:97], v182 offset:43264
	s_waitcnt lgkmcnt(0)
	v_mfma_f32_16x16x32_bf16 v[38:41], v[94:97], v[90:93], v[38:41]
	ds_read_b64_tr_b16 v[94:95], v183 offset:43008
	ds_read_b64_tr_b16 v[96:97], v184 offset:43264
	s_waitcnt lgkmcnt(0)
	v_mfma_f32_16x16x32_bf16 v[34:37], v[94:97], v[90:93], v[34:37]
	ds_read_b64_tr_b16 v[94:95], v181 offset:43520
	ds_read_b64_tr_b16 v[96:97], v182 offset:43776
	s_waitcnt lgkmcnt(0)
	v_mfma_f32_16x16x32_bf16 v[30:33], v[94:97], v[90:93], v[30:33]
	ds_read_b64_tr_b16 v[94:95], v183 offset:43520
	ds_read_b64_tr_b16 v[96:97], v184 offset:43776
	s_waitcnt lgkmcnt(0)
	v_mfma_f32_16x16x32_bf16 v[26:29], v[94:97], v[90:93], v[26:29]
	ds_read_b64_tr_b16 v[94:95], v181 offset:44032
	ds_read_b64_tr_b16 v[96:97], v182 offset:44288
	s_waitcnt lgkmcnt(0)
	v_mfma_f32_16x16x32_bf16 v[18:21], v[94:97], v[90:93], v[18:21]
	ds_read_b64_tr_b16 v[94:95], v183 offset:44032
	ds_read_b64_tr_b16 v[96:97], v184 offset:44288
	s_waitcnt lgkmcnt(0)
	v_mfma_f32_16x16x32_bf16 v[14:17], v[94:97], v[90:93], v[14:17]
	ds_read_b64_tr_b16 v[94:95], v181 offset:44544
	ds_read_b64_tr_b16 v[96:97], v182 offset:44800
	s_waitcnt lgkmcnt(0)
	v_mfma_f32_16x16x32_bf16 v[10:13], v[94:97], v[90:93], v[10:13]
	ds_read_b64_tr_b16 v[94:95], v183 offset:44544
	ds_read_b64_tr_b16 v[96:97], v184 offset:44800
	s_waitcnt lgkmcnt(0)
	s_barrier
; #define LAS __attribute__((address_space(3)))
; __device__ __forceinline__ void ret_r3_phase(LAS unsigned char* lds, const bf16_t* proj, const float* cosT, const float* sinT, const float* gst, bf16_t* ycat, int G, int b) {
;     ...
;                 float v[16]; float sum = 0.f;
; #pragma unroll
;                 for (int q = 0; q < 4; ++q) { const f32x4 t = *(const LAS f32x4*)(OS + m * 132 + tq * 16 + q * 4); v[4 * q] = t.x; v[4 * q + 1] = t.y; v[4 * q + 2] = t.z; v[4 * q + 3] = t.w; sum += (t.x + t.y) + (t.z + t.w); }
;                 sum += __shfl_xor(sum, 1); sum += __shfl_xor(sum, 2); sum += __shfl_xor(sum, 4);
;                 const float mean = sum * (1.0f / 128.0f); float sq = 0.f;
; #pragma unroll
;                 for (int q = 0; q < 16; ++q) { v[q] -= mean; sq += v[q] * v[q]; }
;                 sq += __shfl_xor(sq, 1); sq += __shfl_xor(sq, 2); sq += __shfl_xor(sq, 4);
;                 const float rstd = 1.0f / sqrtf(sq * (1.0f / 128.0f) + GN_EPS);
	v_mfma_f32_16x16x32_bf16 v[6:9], v[94:97], v[90:93], v[6:9]
	ds_read_b128 v[102:105], v200
	ds_read_b128 v[98:101], v200 offset:16
	ds_read_b128 v[94:97], v200 offset:32
	ds_read_b128 v[90:93], v200 offset:48
	s_waitcnt lgkmcnt(3)
	v_mov_b32_e32 v230, v103
	v_mov_b32_e32 v231, v104
	v_mov_b32_e32 v232, v102
	v_mov_b32_e32 v233, v105
	v_pk_add_f32 v[230:231], v[230:231], v[232:233]
	s_waitcnt lgkmcnt(2)
	v_mov_b32_e32 v232, v99
	v_mov_b32_e32 v233, v100
	v_mov_b32_e32 v234, v98
	v_mov_b32_e32 v235, v101
	v_pk_add_f32 v[232:233], v[232:233], v[234:235]
	v_add_f32_e32 v141, v230, v231
	v_pk_add_f32 v[232:233], v[232:233], v[232:233] op_sel:[0,1] op_sel_hi:[1,0]
	v_add_f32_e32 v230, 0, v141
	s_waitcnt lgkmcnt(1)
	v_add_f32_e32 v234, v94, v95
	v_add_f32_e32 v236, v96, v97
	s_waitcnt lgkmcnt(0)
	v_mov_b32_e32 v231, v90
	v_mov_b32_e32 v233, v91
	v_mov_b32_e32 v235, v92
	v_mov_b32_e32 v237, v93
	v_pk_add_f32 v[230:231], v[230:231], v[232:233]
	v_pk_add_f32 v[232:233], v[234:235], v[236:237]
	v_xor_b32_e32 v141, 1, v201
	v_pk_add_f32 v[230:231], v[230:231], v[232:233]
	s_nop 0
	v_add_f32_e32 v145, v230, v231
	v_and_b32_e32 v230, 64, v201
	v_add_u32_e32 v231, 64, v230
	v_cmp_lt_i32_e32 vcc, v141, v231
	s_nop 1
	v_cndmask_b32_e32 v141, v201, v141, vcc
	v_lshlrev_b32_e32 v141, 2, v141
	s_nop 1
	s_waitcnt lgkmcnt(0)
	v_add_f32_dpp v145, v145, v145 quad_perm:[1,0,3,2] row_mask:0xf bank_mask:0xf
	v_xor_b32_e32 v230, 2, v201
	v_cmp_lt_i32_e32 vcc, v230, v231
	s_nop 1
	v_cndmask_b32_e32 v230, v201, v230, vcc
	v_lshlrev_b32_e32 v230, 2, v230
	s_nop 1
	s_waitcnt lgkmcnt(0)
	v_add_f32_dpp v145, v145, v145 quad_perm:[2,3,0,1] row_mask:0xf bank_mask:0xf
	v_xor_b32_e32 v232, 4, v201
	v_cmp_lt_i32_e32 vcc, v232, v231
	s_nop 1
	v_cndmask_b32_e32 v231, v201, v232, vcc
	v_lshlrev_b32_e32 v231, 2, v231
	s_nop 1
	s_waitcnt lgkmcnt(0)
	v_add_f32_dpp v145, v145, v145 row_half_mirror row_mask:0xf bank_mask:0xf
	v_fmamk_f32 v235, v145, 0xbc000000, v103
	v_fmamk_f32 v234, v145, 0xbc000000, v102
	v_mul_f32_e32 v236, v235, v235
	v_fmac_f32_e32 v236, v234, v234
	v_fmamk_f32 v104, v145, 0xbc000000, v104
	v_fmac_f32_e32 v236, v104, v104
	v_fmac_f32_e32 v105, 0xbc000000, v145
	v_fmac_f32_e32 v236, v105, v105
	v_fmamk_f32 v103, v145, 0xbc000000, v98
	v_fmac_f32_e32 v236, v103, v103
	v_fmamk_f32 v102, v145, 0xbc000000, v99
	v_fmac_f32_e32 v236, v102, v102
	v_fmamk_f32 v100, v145, 0xbc000000, v100
	v_fmac_f32_e32 v236, v100, v100
	v_fmac_f32_e32 v101, 0xbc000000, v145
	v_fmac_f32_e32 v236, v101, v101
	v_fmamk_f32 v99, v145, 0xbc000000, v94
	v_fmac_f32_e32 v236, v99, v99
	v_fmamk_f32 v98, v145, 0xbc000000, v95
	v_fmac_f32_e32 v236, v98, v98
	v_fmamk_f32 v95, v145, 0xbc000000, v96
	v_fmac_f32_e32 v236, v95, v95
	v_fmac_f32_e32 v97, 0xbc000000, v145
	v_mul_f32_e32 v232, 0x3c000000, v145
	v_fmac_f32_e32 v236, v97, v97
	v_fmamk_f32 v94, v145, 0xbc000000, v90
	v_fmac_f32_e32 v236, v94, v94
	v_fmac_f32_e32 v91, 0xbc000000, v145
	v_pk_add_f32 v[92:93], v[92:93], v[232:233] op_sel_hi:[1,0] neg_lo:[0,1] neg_hi:[0,1]
	v_fmac_f32_e32 v236, v91, v91
	v_pk_mul_f32 v[232:233], v[92:93], v[92:93]
	s_nop 0
	v_add_f32_e32 v90, v232, v236
	v_add_f32_e32 v90, v233, v90
	s_nop 1
	s_waitcnt lgkmcnt(0)
	v_add_f32_dpp v90, v90, v90 quad_perm:[1,0,3,2] row_mask:0xf bank_mask:0xf
	s_nop 1
	s_waitcnt lgkmcnt(0)
	v_add_f32_dpp v90, v90, v90 quad_perm:[2,3,0,1] row_mask:0xf bank_mask:0xf
	s_nop 1
	s_waitcnt lgkmcnt(0)
	v_add_f32_dpp v90, v90, v90 row_half_mirror row_mask:0xf bank_mask:0xf
	v_fmamk_f32 v90, v90, 0x3c000000, v185
	v_cmp_gt_f32_e32 vcc, s6, v90
	v_mul_f32_e32 v96, 0x4f800000, v90
	s_nop 0
	v_cndmask_b32_e32 v90, v90, v96, vcc
	v_sqrt_f32_e32 v96, v90
	s_nop 0
	v_add_u32_e32 v145, -1, v96
	v_fma_f32 v232, -v145, v96, v90
	v_cmp_ge_f32_e64 s[0:1], 0, v232
	v_add_u32_e32 v232, 1, v96
	s_nop 0
	v_cndmask_b32_e64 v145, v96, v145, s[0:1]
	v_fma_f32 v96, -v232, v96, v90
	v_cmp_lt_f32_e64 s[0:1], 0, v96
	s_nop 1
	v_cndmask_b32_e64 v96, v145, v232, s[0:1]
	v_mul_f32_e32 v145, 0x37800000, v96
	v_cndmask_b32_e32 v96, v96, v145, vcc
	v_cmp_class_f32_e32 vcc, v90, v186
	s_nop 1
	v_cndmask_b32_e32 v90, v96, v90, vcc
	v_div_scale_f32 v96, s[0:1], v90, v90, 1.0
	v_rcp_f32_e32 v145, v96
	s_nop 0
	v_fma_f32 v232, -v96, v145, 1.0
	v_fmac_f32_e32 v145, v232, v145
	v_div_scale_f32 v232, vcc, 1.0, v90, 1.0
	v_mul_f32_e32 v233, v232, v145
	v_fma_f32 v236, -v96, v233, v232
	v_fmac_f32_e32 v233, v236, v145
	v_fma_f32 v96, -v96, v233, v232
	v_div_fmas_f32 v96, v96, v145, v233
	v_div_fixup_f32 v90, v96, v90, 1.0
	v_lshlrev_b32_e32 v96, 16, v86
	v_and_b32_e32 v145, 0xffff0000, v86
	v_mul_f32_e32 v86, 0xbfb8aa3b, v96
	v_exp_f32_e32 v86, v86
	s_nop 0
	v_add_f32_e32 v86, 1.0, v86
	v_rcp_f32_e32 v86, v86
	s_nop 0
	v_mul_f32_e32 v86, v86, v96
	v_mul_f32_e32 v96, 0xbfb8aa3b, v145
	v_exp_f32_e32 v96, v96
	v_mul_f32_e32 v86, v86, v234
	v_mul_f32_e32 v86, v86, v90
	v_add_f32_e32 v96, 1.0, v96
	v_rcp_f32_e32 v96, v96
	s_nop 0
	v_mul_f32_e32 v96, v96, v145
	v_lshlrev_b32_e32 v145, 16, v87
	v_mul_f32_e32 v232, 0xbfb8aa3b, v145
	v_exp_f32_e32 v232, v232
	v_and_b32_e32 v87, 0xffff0000, v87
	v_mul_f32_e32 v96, v96, v235
	v_mul_f32_e32 v96, v96, v90
	v_add_f32_e32 v232, 1.0, v232
	v_rcp_f32_e32 v232, v232
	s_nop 0
	v_mul_f32_e32 v145, v232, v145
	v_mul_f32_e32 v104, v145, v104
	v_mul_f32_e32 v145, 0xbfb8aa3b, v87
	v_exp_f32_e32 v145, v145
	v_mul_f32_e32 v104, v104, v90
	v_add_f32_e32 v145, 1.0, v145
	v_rcp_f32_e32 v145, v145
	s_nop 0
	v_mul_f32_e32 v87, v145, v87
	v_mul_f32_e32 v87, v87, v105
	v_lshlrev_b32_e32 v105, 16, v88
	v_mul_f32_e32 v145, 0xbfb8aa3b, v105
	v_exp_f32_e32 v145, v145
	v_and_b32_e32 v88, 0xffff0000, v88
	v_mul_f32_e32 v87, v87, v90
	v_med3_f32 v87, v87, s7, v213
	v_add_f32_e32 v145, 1.0, v145
	v_rcp_f32_e32 v145, v145
	s_nop 0
	v_mul_f32_e32 v105, v145, v105
	v_mul_f32_e32 v103, v105, v103
	v_mul_f32_e32 v105, 0xbfb8aa3b, v88
	v_exp_f32_e32 v105, v105
	v_mul_f32_e32 v103, v103, v90
	v_ashrrev_i32_e32 v145, 31, v144
	v_add_f32_e32 v105, 1.0, v105
	v_rcp_f32_e32 v105, v105
	s_nop 0
	v_mul_f32_e32 v88, v105, v88
	v_mul_f32_e32 v88, v88, v102
	v_lshlrev_b32_e32 v102, 16, v89
	v_mul_f32_e32 v105, 0xbfb8aa3b, v102
	v_exp_f32_e32 v105, v105
	v_and_b32_e32 v89, 0xffff0000, v89
	v_mul_f32_e32 v88, v88, v90
	v_add_f32_e32 v105, 1.0, v105
	v_rcp_f32_e32 v105, v105
	s_nop 0
	v_mul_f32_e32 v102, v105, v102
	v_mul_f32_e32 v100, v102, v100
	v_mul_f32_e32 v102, 0xbfb8aa3b, v89
	v_exp_f32_e32 v102, v102
	v_mul_f32_e32 v100, v100, v90
	v_add_f32_e32 v102, 1.0, v102
	v_rcp_f32_e32 v102, v102
	s_nop 0
	v_mul_f32_e32 v89, v102, v89
	v_mul_f32_e32 v89, v89, v101
	s_waitcnt vmcnt(12)
; #define LAS __attribute__((address_space(3)))
; __device__ __forceinline__ unsigned pk2(float lo, float hi) { const f32x2c_t v = {lo, hi}; const bf16x2c_t b = __builtin_convertvector(v, bf16x2c_t); return __builtin_bit_cast(unsigned, b); }
; __device__ __forceinline__ float bflo(unsigned w) { return __uint_as_float(w << 16); }
; __device__ __forceinline__ float bfhi(unsigned w) { return __uint_as_float(w & 0xffff0000u); }
; __device__ __forceinline__ float sigmoidf_(float x) { return __builtin_amdgcn_rcpf(1.0f + fexp_(-x)); }
; __device__ __forceinline__ void ret_r3_phase(LAS unsigned char* lds, const bf16_t* proj, const float* cosT, const float* sinT, const float* gst, bf16_t* ycat, int G, int b) {
;     ...
;                 rot8r(pn.q1, pn.q2, pn, 0.08838834764831845f, o1, o2);
;                 *(LAS u32x4*)(QS + m * 136 + tq * 8) = (u32x4){pk2(o1[0], o1[1]), pk2(o1[2], o1[3]), pk2(o1[4], o1[5]), pk2(o1[6], o1[7])};
;                 *(LAS u32x4*)(QS + m * 136 + 64 + tq * 8) = (u32x4){pk2(o2[0], o2[1]), pk2(o2[2], o2[3]), pk2(o2[4], o2[5]), pk2(o2[6], o2[7])};
;                 ret_stage_kv(pn, KT, VT, m, tq, kdec, o1, o2);
;                 *(LAS u32x4*)(KS + m * 136 + tq * 8) = (u32x4){pk2(o1[0], o1[1]), pk2(o1[2], o1[3]), pk2(o1[4], o1[5]), pk2(o1[6], o1[7])};
;                 *(LAS u32x4*)(KS + m * 136 + 64 + tq * 8) = (u32x4){pk2(o2[0], o2[1]), pk2(o2[2], o2[3]), pk2(o2[4], o2[5]), pk2(o2[6], o2[7])};
;     ...
;                     for (int j = 0; j < 8; ++j) { const float ga = bflo(gw[j]), gb = bfhi(gw[j]); y[2 * j] = ga * sigmoidf_(ga) * v[2 * j] * rstd; y[2 * j + 1] = gb * sigmoidf_(gb) * v[2 * j + 1] * rstd; }
;                     *(u32x4*)((unsigned char*)ycat + (size_t)s * D_ + h * 128 + tq * 16) = (u32x4){pk4_fp8(y[0], y[1], y[2], y[3]), pk4_fp8(y[4], y[5], y[6], y[7]), pk4_fp8(y[8], y[9], y[10], y[11]), pk4_fp8(y[12], y[13], y[14], y[15])};
	v_lshlrev_b32_e32 v101, 16, v82
	v_mul_f32_e32 v102, 0xbfb8aa3b, v101
	v_exp_f32_e32 v102, v102
	v_and_b32_e32 v82, 0xffff0000, v82
	v_mul_f32_e32 v89, v89, v90
	v_add_f32_e32 v102, 1.0, v102
	v_rcp_f32_e32 v102, v102
	s_nop 0
	v_mul_f32_e32 v101, v102, v101
	v_mul_f32_e32 v99, v101, v99
	v_mul_f32_e32 v101, 0xbfb8aa3b, v82
	v_exp_f32_e32 v101, v101
	v_mul_f32_e32 v99, v99, v90
	v_add_f32_e32 v101, 1.0, v101
	v_rcp_f32_e32 v101, v101
	s_nop 0
	v_mul_f32_e32 v82, v101, v82
	v_mul_f32_e32 v82, v82, v98
	v_mul_f32_e32 v98, v82, v90
	v_lshlrev_b32_e32 v82, 16, v83
	v_mul_f32_e32 v101, 0xbfb8aa3b, v82
	v_exp_f32_e32 v101, v101
	v_and_b32_e32 v83, 0xffff0000, v83
	v_add_f32_e32 v101, 1.0, v101
	v_rcp_f32_e32 v101, v101
	s_nop 0
	v_mul_f32_e32 v82, v101, v82
	v_mul_f32_e32 v82, v82, v95
	v_mul_f32_e32 v95, v82, v90
	v_mul_f32_e32 v82, 0xbfb8aa3b, v83
	v_exp_f32_e32 v82, v82
	s_nop 0
	v_add_f32_e32 v82, 1.0, v82
	v_rcp_f32_e32 v82, v82
	s_nop 0
	v_mul_f32_e32 v82, v82, v83
	v_mul_f32_e32 v82, v82, v97
	v_mul_f32_e32 v97, v82, v90
	v_lshlrev_b32_e32 v82, 16, v84
	v_and_b32_e32 v83, 0xffff0000, v84
	v_mul_f32_e32 v84, 0xbfb8aa3b, v82
	v_exp_f32_e32 v84, v84
	s_nop 0
	v_add_f32_e32 v84, 1.0, v84
	v_rcp_f32_e32 v84, v84
	s_nop 0
	v_mul_f32_e32 v82, v84, v82
	v_mul_f32_e32 v82, v82, v94
	v_mul_f32_e32 v94, v82, v90
	v_mul_f32_e32 v82, 0xbfb8aa3b, v83
	v_exp_f32_e32 v82, v82
	s_nop 0
	v_add_f32_e32 v82, 1.0, v82
	v_rcp_f32_e32 v82, v82
	s_nop 0
	v_mul_f32_e32 v82, v82, v83
	v_mul_f32_e32 v82, v82, v91
	v_mul_f32_e32 v91, v82, v90
	v_lshlrev_b32_e32 v82, 16, v85
	v_mul_f32_e32 v84, 0xbfb8aa3b, v82
	v_exp_f32_e32 v84, v84
	v_and_b32_e32 v83, 0xffff0000, v85
	v_add_f32_e32 v84, 1.0, v84
	v_rcp_f32_e32 v84, v84
	s_nop 0
	v_mul_f32_e32 v82, v84, v82
	v_mul_f32_e32 v82, v82, v92
	v_mul_f32_e32 v85, v82, v90
	v_mul_f32_e32 v82, 0xbfb8aa3b, v83
	v_exp_f32_e32 v82, v82
	v_med3_f32 v84, v96, s7, v213
	v_add_f32_e32 v82, 1.0, v82
	v_rcp_f32_e32 v82, v82
	s_nop 0
	v_mul_f32_e32 v82, v82, v83
	v_mul_f32_e32 v82, v82, v93
	v_mul_f32_e32 v90, v82, v90
	v_med3_f32 v83, v86, s7, v213
	v_mov_b32_e32 v82, 0
	v_cvt_pk_fp8_f32 v82, v83, v84
	v_med3_f32 v86, v104, s7, v213
	v_med3_f32 v84, v103, s7, v213
	v_mov_b32_e32 v83, 0
	v_cvt_pk_fp8_f32 v82, v86, v87 op_sel:[0,0,1]
	v_med3_f32 v86, v88, s7, v213
	v_cvt_pk_fp8_f32 v83, v84, v86
	v_med3_f32 v87, v100, s7, v213
	v_med3_f32 v88, v89, s7, v213
	v_med3_f32 v86, v99, s7, v213
	v_cvt_pk_fp8_f32 v83, v87, v88 op_sel:[0,0,1]
	v_med3_f32 v87, v98, s7, v213
	v_mov_b32_e32 v84, 0
	v_cvt_pk_fp8_f32 v84, v86, v87
	v_med3_f32 v88, v95, s7, v213
	v_med3_f32 v89, v97, s7, v213
	v_med3_f32 v86, v94, s7, v213
	v_cvt_pk_fp8_f32 v84, v88, v89 op_sel:[0,0,1]
	v_med3_f32 v87, v91, s7, v213
	v_med3_f32 v88, v85, s7, v213
	v_mov_b32_e32 v85, 0
	v_cvt_pk_fp8_f32 v85, v86, v87
	v_med3_f32 v89, v90, s7, v213
	v_lshlrev_b64 v[86:87], 11, v[144:145]
	v_lshl_add_u64 v[86:87], v[120:121], 0, v[86:87]
	v_cvt_pk_fp8_f32 v85, v88, v89 op_sel:[0,0,1]
	global_store_dwordx4 v[86:87], v[82:85], off
	s_waitcnt vmcnt(1)
	s_nop 0
	v_mov_b64_e32 v[84:85], v[4:5]
	v_mov_b64_e32 v[88:89], v[24:25]
	v_mov_b64_e32 v[82:83], v[2:3]
	v_mov_b64_e32 v[86:87], v[22:23]
	s_cbranch_scc0 .LBB0_405
	v_lshlrev_b32_e32 v82, 16, v78
	v_and_b32_e32 v83, 0xffff0000, v78
	v_lshlrev_b32_e32 v84, 16, v74
	v_and_b32_e32 v85, 0xffff0000, v74
	v_pk_mul_f32 v[86:87], v[66:67], v[82:83]
	v_pk_mul_f32 v[82:83], v[70:71], v[82:83]
	v_lshlrev_b32_e32 v78, 16, v79
	v_and_b32_e32 v79, 0xffff0000, v79
	v_pk_fma_f32 v[86:87], v[70:71], v[84:85], v[86:87] neg_lo:[0,0,1] neg_hi:[0,0,1]
	v_pk_fma_f32 v[82:83], v[66:67], v[84:85], v[82:83]
	v_lshlrev_b32_e32 v74, 16, v75
	v_and_b32_e32 v75, 0xffff0000, v75
	v_pk_mul_f32 v[84:85], v[68:69], v[78:79]
	v_pk_mul_f32 v[78:79], v[72:73], v[78:79]
	v_pk_fma_f32 v[84:85], v[72:73], v[74:75], v[84:85] neg_lo:[0,0,1] neg_hi:[0,0,1]
	v_pk_fma_f32 v[74:75], v[68:69], v[74:75], v[78:79]
	v_lshlrev_b32_e32 v88, 16, v76
	v_pk_mul_f32 v[78:79], v[74:75], s[54:55] op_sel_hi:[1,0]
	v_lshlrev_b32_e32 v74, 16, v80
	v_and_b32_e32 v75, 0xffff0000, v80
	v_and_b32_e32 v89, 0xffff0000, v76
	v_pk_mul_f32 v[90:91], v[62:63], v[74:75]
	v_pk_mul_f32 v[74:75], v[50:51], v[74:75]
	v_pk_fma_f32 v[90:91], v[50:51], v[88:89], v[90:91] neg_lo:[0,0,1] neg_hi:[0,0,1]
	v_pk_fma_f32 v[74:75], v[62:63], v[88:89], v[74:75]
	v_lshlrev_b32_e32 v76, 16, v77
	v_pk_mul_f32 v[88:89], v[74:75], s[54:55] op_sel_hi:[1,0]
	v_lshlrev_b32_e32 v74, 16, v81
	v_and_b32_e32 v75, 0xffff0000, v81
	v_and_b32_e32 v77, 0xffff0000, v77
	v_pk_mul_f32 v[80:81], v[64:65], v[74:75]
	v_pk_mul_f32 v[74:75], v[52:53], v[74:75]
	v_pk_fma_f32 v[80:81], v[52:53], v[76:77], v[80:81] neg_lo:[0,0,1] neg_hi:[0,0,1]
	v_pk_mul_f32 v[86:87], v[86:87], s[54:55] op_sel_hi:[1,0]
	v_pk_mul_f32 v[84:85], v[84:85], s[54:55] op_sel_hi:[1,0]
	v_pk_mul_f32 v[90:91], v[90:91], s[54:55] op_sel_hi:[1,0]
	v_pk_mul_f32 v[80:81], v[80:81], s[54:55] op_sel_hi:[1,0]
	v_pk_fma_f32 v[74:75], v[64:65], v[76:77], v[74:75]
	v_pk_mul_f32 v[82:83], v[82:83], s[54:55] op_sel_hi:[1,0]
	v_pk_mul_f32 v[92:93], v[74:75], s[54:55] op_sel_hi:[1,0]
	v_cvt_pk_bf16_f32 v74, v86, v87
	v_cvt_pk_bf16_f32 v75, v84, v85
	v_cvt_pk_bf16_f32 v76, v90, v91
	v_cvt_pk_bf16_f32 v77, v80, v81
	ds_write_b128 v147, v[74:77]
	v_cvt_pk_bf16_f32 v74, v82, v83
	v_cvt_pk_bf16_f32 v75, v78, v79
	v_cvt_pk_bf16_f32 v76, v88, v89
	v_cvt_pk_bf16_f32 v77, v92, v93
	ds_write_b128 v147, v[74:77] offset:128
	v_lshlrev_b32_e32 v74, 16, v58
	v_and_b32_e32 v75, 0xffff0000, v58
	v_lshlrev_b32_e32 v76, 16, v54
	v_and_b32_e32 v77, 0xffff0000, v54
	v_pk_mul_f32 v[78:79], v[66:67], v[74:75]
; #define LAS __attribute__((address_space(3)))
; __device__ __forceinline__ void ret_r3_phase(LAS unsigned char* lds, const bf16_t* proj, const float* cosT, const float* sinT, const float* gst, bf16_t* ycat, int G, int b) {
;     ...
;                 ret_stage_kv(pn, KT, VT, m, tq, kdec, o1, o2);
;                 *(LAS u32x4*)(KS + m * 136 + tq * 8) = (u32x4){pk2(o1[0], o1[1]), pk2(o1[2], o1[3]), pk2(o1[4], o1[5]), pk2(o1[6], o1[7])};
;                 *(LAS u32x4*)(KS + m * 136 + 64 + tq * 8) = (u32x4){pk2(o2[0], o2[1]), pk2(o2[2], o2[3]), pk2(o2[4], o2[5]), pk2(o2[6], o2[7])};
;             }
;             if (i + 1 < 8) ret_prefetch<true>(pn, proj, cosT, sinT, s + 64, h, tq);
;             __syncthreads();
;             f32x4 oacc[4];
;             {
;                 const int ct = wid & 3, mt0 = (wid >> 2) * 2;
;                 f32x4 sacc[2] = {(f32x4){0.f, 0.f, 0.f, 0.f}, (f32x4){0.f, 0.f, 0.f, 0.f}};
; #pragma unroll
;                 for (int ks = 0; ks < 4; ++ks) {
;                     const bf16x8 a = *(const LAS bf16x8*)(QS + (ct * 16 + fr) * 136 + ks * 32 + fq * 8);
; #pragma unroll
;                     for (int j = 0; j < 2; ++j) { const bf16x8 bb = *(const LAS bf16x8*)(KS + ((mt0 + j) * 16 + fr) * 136 + ks * 32 + fq * 8); sacc[j] = mfma16(a, bb, sacc[j]); }
;                 }
; #pragma unroll
;                 for (int j = 0; j < 2; ++j)
; #pragma unroll
;                     for (int r = 0; r < 4; ++r) { const int c = ct * 16 + fq * 4 + r, mm = (mt0 + j) * 16 + fr;
;                         PS[c * 72 + mm] = (bf16_t)f2bf(sacc[j][r] * pdec[j][r]); }
;                 asm volatile("" ::: "memory");
; #pragma unroll
;                 for (int c4 = 0; c4 < 4; ++c4) oacc[c4] = (f32x4){0.f, 0.f, 0.f, 0.f};
; #pragma unroll
;                 for (int a4 = 0; a4 < 4; ++a4) {
;                     u32x4 bw; bw.x = pk2(S[2 * a4][0], S[2 * a4][1]); bw.y = pk2(S[2 * a4][2], S[2 * a4][3]); bw.z = pk2(S[2 * a4 + 1][0], S[2 * a4 + 1][1]); bw.w = pk2(S[2 * a4 + 1][2], S[2 * a4 + 1][3]);
;                     const bf16x8 bb = __builtin_bit_cast(bf16x8, bw);
; #pragma unroll
;                     for (int c4 = 0; c4 < 4; ++c4) {
;                         const u32x2 lo = *(const LAS u32x2*)(QS + (c4 * 16 + fr) * 136 + a4 * 32 + fq * 4), hi = *(const LAS u32x2*)(QS + (c4 * 16 + fr) * 136 + a4 * 32 + 16 + fq * 4);
	v_lshlrev_b32_e32 v58, 16, v59
	v_pk_fma_f32 v[78:79], v[70:71], v[76:77], v[78:79] neg_lo:[0,0,1] neg_hi:[0,0,1]
	v_and_b32_e32 v59, 0xffff0000, v59
	v_pk_mul_f32 v[80:81], v[138:139], v[78:79]
	v_pk_mul_f32 v[82:83], v[68:69], v[58:59]
	v_cvt_pk_bf16_f32 v54, v80, v81
	v_lshlrev_b32_e32 v80, 16, v55
	v_and_b32_e32 v81, 0xffff0000, v55
	v_pk_fma_f32 v[82:83], v[72:73], v[80:81], v[82:83] neg_lo:[0,0,1] neg_hi:[0,0,1]
	v_lshlrev_b32_e32 v86, 16, v56
	v_pk_mul_f32 v[84:85], v[138:139], v[82:83]
	v_and_b32_e32 v87, 0xffff0000, v56
	v_cvt_pk_bf16_f32 v55, v84, v85
	v_lshlrev_b32_e32 v84, 16, v60
	v_and_b32_e32 v85, 0xffff0000, v60
	v_pk_mul_f32 v[88:89], v[62:63], v[84:85]
	v_lshlrev_b32_e32 v60, 16, v61
	v_pk_fma_f32 v[88:89], v[50:51], v[86:87], v[88:89] neg_lo:[0,0,1] neg_hi:[0,0,1]
	v_and_b32_e32 v61, 0xffff0000, v61
	v_pk_mul_f32 v[90:91], v[138:139], v[88:89]
	v_pk_mul_f32 v[92:93], v[64:65], v[60:61]
	v_cvt_pk_bf16_f32 v56, v90, v91
	v_lshlrev_b32_e32 v90, 16, v57
	v_and_b32_e32 v91, 0xffff0000, v57
	v_pk_fma_f32 v[92:93], v[52:53], v[90:91], v[92:93] neg_lo:[0,0,1] neg_hi:[0,0,1]
	s_or_b32 s0, s39, 0x1c0
	v_pk_mul_f32 v[94:95], v[138:139], v[92:93]
	v_cvt_pk_bf16_f32 v38, v38, v39
	v_cvt_pk_bf16_f32 v57, v94, v95
	ds_write_b128 v189, v[54:57] offset:34816
	v_pk_mul_f32 v[54:55], v[66:67], v[76:77]
	v_pk_mul_f32 v[56:57], v[68:69], v[80:81]
	v_pk_fma_f32 v[66:67], v[70:71], v[74:75], v[54:55]
	v_pk_fma_f32 v[58:59], v[72:73], v[58:59], v[56:57]
	v_pk_mul_f32 v[54:55], v[138:139], v[66:67]
	v_pk_mul_f32 v[56:57], v[138:139], v[58:59]
	v_cvt_pk_bf16_f32 v54, v54, v55
	v_cvt_pk_bf16_f32 v55, v56, v57
	v_pk_mul_f32 v[56:57], v[62:63], v[86:87]
	v_pk_mul_f32 v[62:63], v[64:65], v[90:91]
	v_pk_fma_f32 v[50:51], v[50:51], v[84:85], v[56:57]
	v_pk_fma_f32 v[52:53], v[52:53], v[60:61], v[62:63]
	v_pk_mul_f32 v[56:57], v[138:139], v[50:51]
	v_pk_mul_f32 v[60:61], v[138:139], v[52:53]
	v_cvt_pk_bf16_f32 v56, v56, v57
	v_cvt_pk_bf16_f32 v57, v60, v61
	ds_write_b128 v189, v[54:57] offset:35840
	ds_write_b128 v190, v[46:49] offset:53248
	ds_write_b128 v191, v[42:45] offset:53248
	v_cvt_pk_bf16_f32 v42, v78, v79
	v_cvt_pk_bf16_f32 v43, v82, v83
	v_cvt_pk_bf16_f32 v44, v88, v89
	v_cvt_pk_bf16_f32 v45, v92, v93
	ds_write_b128 v147, v[42:45] offset:17408
	v_cvt_pk_bf16_f32 v42, v66, v67
	v_cvt_pk_bf16_f32 v43, v58, v59
	v_cvt_pk_bf16_f32 v44, v50, v51
	v_cvt_pk_bf16_f32 v45, v52, v53
	ds_write_b128 v147, v[42:45] offset:17536
	s_waitcnt lgkmcnt(0)
	s_barrier
	ds_read_b128 v[44:47], v148
	ds_read_b128 v[48:51], v192 offset:17408
	ds_read_b128 v[52:55], v193 offset:17408
	s_waitcnt lgkmcnt(1)
	v_mfma_f32_16x16x32_bf16 v[48:51], v[44:47], v[48:51], 0
	v_cvt_pk_bf16_f32 v39, v40, v41
	v_cvt_pk_bf16_f32 v40, v34, v35
	v_cvt_pk_bf16_f32 v41, v36, v37
	s_waitcnt lgkmcnt(0)
	v_mfma_f32_16x16x32_bf16 v[44:47], v[44:47], v[52:55], 0
	ds_read_b128 v[52:55], v148 offset:64
	ds_read_b128 v[56:59], v192 offset:17472
	v_cvt_pk_bf16_f32 v30, v30, v31
	v_cvt_pk_bf16_f32 v31, v32, v33
	s_waitcnt lgkmcnt(0)
	v_mfma_f32_16x16x32_bf16 v[48:51], v[52:55], v[56:59], v[48:51]
	ds_read_b128 v[56:59], v193 offset:17472
	v_cvt_pk_bf16_f32 v32, v26, v27
	v_cvt_pk_bf16_f32 v33, v28, v29
	s_waitcnt lgkmcnt(0)
	v_mfma_f32_16x16x32_bf16 v[44:47], v[52:55], v[56:59], v[44:47]
	ds_read_b128 v[52:55], v148 offset:128
	ds_read_b128 v[56:59], v192 offset:17536
	v_cvt_pk_bf16_f32 v18, v18, v19
	v_cvt_pk_bf16_f32 v19, v20, v21
	s_waitcnt lgkmcnt(0)
	v_mfma_f32_16x16x32_bf16 v[48:51], v[52:55], v[56:59], v[48:51]
	ds_read_b128 v[56:59], v193 offset:17536
	v_cvt_pk_bf16_f32 v20, v14, v15
	v_cvt_pk_bf16_f32 v21, v16, v17
	s_waitcnt lgkmcnt(0)
	v_mfma_f32_16x16x32_bf16 v[44:47], v[52:55], v[56:59], v[44:47]
	ds_read_b128 v[52:55], v148 offset:192
	ds_read_b128 v[56:59], v192 offset:17600
	v_cvt_pk_bf16_f32 v10, v10, v11
	v_cvt_pk_bf16_f32 v11, v12, v13
	s_waitcnt lgkmcnt(0)
	v_mfma_f32_16x16x32_bf16 v[48:51], v[52:55], v[56:59], v[48:51]
	ds_read_b128 v[56:59], v193 offset:17600
	v_cvt_pk_bf16_f32 v12, v6, v7
	v_cvt_pk_bf16_f32 v13, v8, v9
	s_nop 4
	v_mul_f32_e32 v43, v214, v48
	v_cvt_pk_bf16_f32 v43, v43, s0
	ds_write_b16 v194, v43
	v_mul_f32_e32 v43, v215, v49
	v_cvt_pk_bf16_f32 v43, v43, s0
	s_waitcnt lgkmcnt(1)
	v_mfma_f32_16x16x32_bf16 v[44:47], v[52:55], v[56:59], v[44:47]
	ds_write_b16 v194, v43 offset:144
	v_mul_f32_e32 v43, v216, v50
	v_cvt_pk_bf16_f32 v43, v43, s0
	ds_write_b16 v194, v43 offset:288
	v_mul_f32_e32 v43, v217, v51
	v_cvt_pk_bf16_f32 v43, v43, s0
	ds_write_b16 v194, v43 offset:432
	s_nop 0
	v_mul_f32_e32 v43, v218, v44
	v_cvt_pk_bf16_f32 v43, v43, s0
	ds_write_b16 v195, v43
	v_mul_f32_e32 v43, v219, v45
	v_cvt_pk_bf16_f32 v43, v43, s0
	ds_write_b16 v195, v43 offset:144
	v_mul_f32_e32 v43, v220, v46
	v_cvt_pk_bf16_f32 v43, v43, s0
	ds_write_b16 v195, v43 offset:288
	v_mul_f32_e32 v43, v221, v47
	v_cvt_pk_bf16_f32 v43, v43, s0
	ds_write_b16 v195, v43 offset:432
	ds_read2_b64 v[34:37], v177 offset1:4
	ds_read2_b64 v[44:47], v178 offset1:4
	ds_read2_b64 v[48:51], v179 offset1:4
	ds_read2_b64 v[52:55], v180 offset1:4
	ds_read2_b64 v[26:29], v177 offset0:8 offset1:12
	s_waitcnt lgkmcnt(4)
	v_mfma_f32_16x16x32_bf16 v[34:37], v[34:37], v[38:41], 0
	v_add_u32_e32 v42, s0, v111
	v_ashrrev_i32_e32 v43, 31, v42
	s_add_i32 s56, s56, s96
	s_waitcnt lgkmcnt(0)
	v_mfma_f32_16x16x32_bf16 v[26:29], v[26:29], v[30:33], v[34:37]
	s_cmpk_gt_i32 s56, 0xff
	s_nop 1
	ds_read2_b64 v[34:37], v178 offset0:8 offset1:12
	v_mfma_f32_16x16x32_bf16 v[44:47], v[44:47], v[38:41], 0
	s_waitcnt lgkmcnt(0)
; __device__ __forceinline__ void ret_r3_phase(LAS unsigned char* lds, const bf16_t* proj, const float* cosT, const float* sinT, const float* gst, bf16_t* ycat, int G, int b) {
;     ...
;                 for (int a4 = 0; a4 < 4; ++a4) {
;                     u32x4 bw; bw.x = pk2(S[2 * a4][0], S[2 * a4][1]); bw.y = pk2(S[2 * a4][2], S[2 * a4][3]); bw.z = pk2(S[2 * a4 + 1][0], S[2 * a4 + 1][1]); bw.w = pk2(S[2 * a4 + 1][2], S[2 * a4 + 1][3]);
;                     const bf16x8 bb = __builtin_bit_cast(bf16x8, bw);
; #pragma unroll
;                     for (int c4 = 0; c4 < 4; ++c4) {
;                         const u32x2 lo = *(const LAS u32x2*)(QS + (c4 * 16 + fr) * 136 + a4 * 32 + fq * 4), hi = *(const LAS u32x2*)(QS + (c4 * 16 + fr) * 136 + a4 * 32 + 16 + fq * 4);
;                         const bf16x8 a = __builtin_bit_cast(bf16x8, (u32x4){lo.x, lo.y, hi.x, hi.y});
;                         oacc[c4] = mfma16(a, bb, oacc[c4]);
;                     }
;                     asm volatile("" ::: "memory");
;                 }
; #pragma unroll
;                 for (int c4 = 0; c4 < 4; ++c4)
; #pragma unroll
;                     for (int r = 0; r < 4; ++r) oacc[c4][r] *= odec[c4][r];
;             }
;             __syncthreads();
;             {
; #pragma unroll
;                 for (int ks = 0; ks < 2; ++ks) {
;                     const bf16x8 bb = trb_frag((const LAS unsigned char*)VT, (unsigned)lane, wid, ks);
; #pragma unroll
;                     for (int c4 = 0; c4 < 4; ++c4) { const bf16x8 a = *(const LAS bf16x8*)(PS + (c4 * 16 + fr) * 72 + ks * 32 + fq * 8); oacc[c4] = mfma16(a, bb, oacc[c4]); }
;                 }
; #pragma unroll
;                 for (int c4 = 0; c4 < 4; ++c4)
; #pragma unroll
;                     for (int r = 0; r < 4; ++r) OS[(c4 * 16 + fq * 4 + r) * 132 + wid * 16 + fr] = oacc[c4][r];
;                 ret_state_update(S, KT, VT, dec, wid, fr, fq);
;             }
;             __syncthreads();
;             {
;                 float v[16]; float sum = 0.f;
; #pragma unroll
;                 for (int q = 0; q < 4; ++q) { const f32x4 t = *(const LAS f32x4*)(OS + m * 132 + tq * 16 + q * 4); v[4 * q] = t.x; v[4 * q + 1] = t.y; v[4 * q + 2] = t.z; v[4 * q + 3] = t.w; sum += (t.x + t.y) + (t.z + t.w); }
;                 sum += __shfl_xor(sum, 1); sum += __shfl_xor(sum, 2); sum += __shfl_xor(sum, 4);
	v_mfma_f32_16x16x32_bf16 v[34:37], v[34:37], v[30:33], v[44:47]
	s_nop 5
	ds_read2_b64 v[44:47], v179 offset0:8 offset1:12
	v_mfma_f32_16x16x32_bf16 v[48:51], v[48:51], v[38:41], 0
	s_waitcnt lgkmcnt(0)
	v_mfma_f32_16x16x32_bf16 v[44:47], v[44:47], v[30:33], v[48:51]
	s_nop 5
	ds_read2_b64 v[48:51], v180 offset0:8 offset1:12
	ds_read2_b64 v[14:17], v177 offset0:16 offset1:20
	s_waitcnt lgkmcnt(0)
	v_mfma_f32_16x16x32_bf16 v[14:17], v[14:17], v[18:21], v[26:29]
	s_nop 2
	ds_read2_b64 v[26:29], v178 offset0:16 offset1:20
	v_mfma_f32_16x16x32_bf16 v[38:41], v[52:55], v[38:41], 0
	v_mfma_f32_16x16x32_bf16 v[30:33], v[48:51], v[30:33], v[38:41]
	s_waitcnt lgkmcnt(0)
	v_mfma_f32_16x16x32_bf16 v[26:29], v[26:29], v[18:21], v[34:37]
	s_nop 4
	ds_read2_b64 v[38:41], v180 offset0:16 offset1:20
	ds_read2_b64 v[34:37], v179 offset0:16 offset1:20
	ds_read2_b64 v[6:9], v177 offset0:24 offset1:28
	s_waitcnt lgkmcnt(0)
	v_mfma_f32_16x16x32_bf16 v[6:9], v[6:9], v[10:13], v[14:17]
	s_nop 2
	ds_read2_b64 v[14:17], v178 offset0:24 offset1:28
	s_nop 3
	v_pk_mul_f32 v[8:9], v[124:125], v[8:9]
	s_waitcnt lgkmcnt(0)
	v_mfma_f32_16x16x32_bf16 v[14:17], v[14:17], v[10:13], v[26:29]
	s_nop 2
	ds_read2_b64 v[26:29], v179 offset0:24 offset1:28
	v_pk_mul_f32 v[6:7], v[122:123], v[6:7]
	s_nop 2
	v_pk_mul_f32 v[16:17], v[128:129], v[16:17]
	v_mfma_f32_16x16x32_bf16 v[34:37], v[34:37], v[18:21], v[44:47]
	v_mul_f32_e64 v14, v126, v14
	v_mul_f32_e64 v15, v127, v15
	v_mfma_f32_16x16x32_bf16 v[18:21], v[38:41], v[18:21], v[30:33]
	s_nop 2
	ds_read2_b64 v[30:33], v180 offset0:24 offset1:28
	s_waitcnt lgkmcnt(1)
	v_mfma_f32_16x16x32_bf16 v[26:29], v[26:29], v[10:13], v[34:37]
	s_waitcnt lgkmcnt(0)
	s_barrier
	v_mfma_f32_16x16x32_bf16 v[10:13], v[30:33], v[10:13], v[18:21]
	s_nop 4
	v_mul_f32_e64 v20, v132, v28
	v_mul_f32_e64 v21, v133, v29
	v_pk_mul_f32 v[18:19], v[130:131], v[26:27]
	ds_read_b64_tr_b16 v[26:27], v196 offset:53248
	ds_read_b64_tr_b16 v[28:29], v197 offset:53504
	ds_read_b128 v[30:33], v198
	s_waitcnt lgkmcnt(0)
	v_mfma_f32_16x16x32_bf16 v[6:9], v[30:33], v[26:29], v[6:9]
	ds_read_b128 v[30:33], v198 offset:2304
	v_pk_mul_f32 v[12:13], v[136:137], v[12:13]
	v_pk_mul_f32 v[10:11], v[134:135], v[10:11]
	s_waitcnt lgkmcnt(0)
	v_mfma_f32_16x16x32_bf16 v[14:17], v[30:33], v[26:29], v[14:17]
	ds_read_b128 v[30:33], v198 offset:4608
	s_waitcnt lgkmcnt(0)
	v_mfma_f32_16x16x32_bf16 v[18:21], v[30:33], v[26:29], v[18:21]
	ds_read_b128 v[30:33], v198 offset:6912
	s_waitcnt lgkmcnt(0)
	v_mfma_f32_16x16x32_bf16 v[10:13], v[30:33], v[26:29], v[10:13]
	ds_read_b64_tr_b16 v[26:27], v196 offset:61440
	ds_read_b64_tr_b16 v[28:29], v197 offset:61696
	ds_read_b128 v[30:33], v198 offset:64
	s_waitcnt lgkmcnt(0)
	v_mfma_f32_16x16x32_bf16 v[6:9], v[30:33], v[26:29], v[6:9]
	ds_read_b128 v[30:33], v198 offset:2368
	s_waitcnt lgkmcnt(0)
	v_mfma_f32_16x16x32_bf16 v[14:17], v[30:33], v[26:29], v[14:17]
	ds_read_b128 v[30:33], v198 offset:4672
	s_waitcnt lgkmcnt(0)
	v_mfma_f32_16x16x32_bf16 v[18:21], v[30:33], v[26:29], v[18:21]
	ds_read_b128 v[30:33], v198 offset:6976
	s_waitcnt lgkmcnt(0)
	v_mfma_f32_16x16x32_bf16 v[10:13], v[30:33], v[26:29], v[10:13]
	ds_write2_b32 v199, v6, v7 offset1:132
	ds_write2_b32 v223, v8, v9 offset0:8 offset1:140
	ds_write2_b32 v224, v14, v15 offset0:64 offset1:196
	ds_write2_b32 v225, v16, v17 offset0:72 offset1:204
	s_nop 0
	ds_write2_b32 v226, v18, v19 offset1:132
	ds_write2_b32 v227, v20, v21 offset0:8 offset1:140
	s_nop 0
	ds_write2_b32 v228, v10, v11 offset0:64 offset1:196
	ds_write2_b32 v229, v12, v13 offset0:72 offset1:204
	s_waitcnt lgkmcnt(0)
	s_barrier
	ds_read_b128 v[18:21], v200
	ds_read_b128 v[14:17], v200 offset:16
	ds_read_b128 v[10:13], v200 offset:32
	ds_read_b128 v[6:9], v200 offset:48
	s_waitcnt lgkmcnt(3)
	v_mov_b32_e32 v26, v19
	v_mov_b32_e32 v27, v20
	v_mov_b32_e32 v28, v18
	v_mov_b32_e32 v29, v21
	v_pk_add_f32 v[26:27], v[26:27], v[28:29]
	s_waitcnt lgkmcnt(2)
	v_mov_b32_e32 v28, v15
	v_mov_b32_e32 v29, v16
	v_mov_b32_e32 v30, v14
	v_mov_b32_e32 v31, v17
	v_pk_add_f32 v[28:29], v[28:29], v[30:31]
	v_add_f32_e32 v26, v26, v27
	v_pk_add_f32 v[28:29], v[28:29], v[28:29] op_sel:[0,1] op_sel_hi:[1,0]
	v_add_f32_e32 v26, 0, v26
	s_waitcnt lgkmcnt(1)
	v_add_f32_e32 v30, v10, v11
	v_add_f32_e32 v32, v12, v13
	s_waitcnt lgkmcnt(0)
	v_mov_b32_e32 v27, v6
	v_mov_b32_e32 v29, v7
	v_mov_b32_e32 v31, v8
	v_mov_b32_e32 v33, v9
	v_pk_add_f32 v[26:27], v[26:27], v[28:29]
	v_pk_add_f32 v[28:29], v[30:31], v[32:33]
	s_nop 0
	v_pk_add_f32 v[26:27], v[26:27], v[28:29]
	s_nop 0
	v_add_f32_e32 v26, v26, v27
	s_nop 1
	s_waitcnt lgkmcnt(0)
	v_add_f32_dpp v26, v26, v26 quad_perm:[1,0,3,2] row_mask:0xf bank_mask:0xf
	s_nop 1
	s_waitcnt lgkmcnt(0)
	v_add_f32_dpp v26, v26, v26 quad_perm:[2,3,0,1] row_mask:0xf bank_mask:0xf
	s_nop 1
	s_waitcnt lgkmcnt(0)
	v_add_f32_dpp v27, v26, v26 row_half_mirror row_mask:0xf bank_mask:0xf
	v_fmamk_f32 v19, v27, 0xbc000000, v19
	v_fmamk_f32 v18, v27, 0xbc000000, v18
	v_mul_f32_e32 v28, v19, v19
	v_fmac_f32_e32 v28, v18, v18
	v_fmamk_f32 v20, v27, 0xbc000000, v20
	v_fmac_f32_e32 v28, v20, v20
	v_fmac_f32_e32 v21, 0xbc000000, v27
	v_fmac_f32_e32 v28, v21, v21
	v_fmamk_f32 v29, v27, 0xbc000000, v14
	v_fmac_f32_e32 v28, v29, v29
	v_fmamk_f32 v30, v27, 0xbc000000, v15
	v_fmac_f32_e32 v28, v30, v30
	v_fmamk_f32 v16, v27, 0xbc000000, v16
	v_fmac_f32_e32 v28, v16, v16
	v_fmac_f32_e32 v17, 0xbc000000, v27
	v_fmac_f32_e32 v28, v17, v17
	v_fmamk_f32 v31, v27, 0xbc000000, v10
	v_fmac_f32_e32 v28, v31, v31
	v_fmamk_f32 v32, v27, 0xbc000000, v11
	v_fmac_f32_e32 v28, v32, v32
	v_fmamk_f32 v12, v27, 0xbc000000, v12
	v_fmac_f32_e32 v28, v12, v12
	v_fmac_f32_e32 v13, 0xbc000000, v27
	v_mul_f32_e32 v26, 0x3c000000, v27
	v_fmac_f32_e32 v28, v13, v13
	v_fmamk_f32 v11, v27, 0xbc000000, v6
	v_fmac_f32_e32 v28, v11, v11
	v_fmac_f32_e32 v7, 0xbc000000, v27
	v_pk_add_f32 v[8:9], v[8:9], v[26:27] op_sel_hi:[1,0] neg_lo:[0,1] neg_hi:[0,1]
	v_fmac_f32_e32 v28, v7, v7
	v_pk_mul_f32 v[14:15], v[8:9], v[8:9]
	s_nop 0
	v_add_f32_e32 v6, v14, v28
	v_add_f32_e32 v6, v15, v6
	s_nop 1
	s_waitcnt lgkmcnt(0)
; __device__ __forceinline__ unsigned pk2(float lo, float hi) { const f32x2c_t v = {lo, hi}; const bf16x2c_t b = __builtin_convertvector(v, bf16x2c_t); return __builtin_bit_cast(unsigned, b); }
; __device__ __forceinline__ float bflo(unsigned w) { return __uint_as_float(w << 16); }
; __device__ __forceinline__ float bfhi(unsigned w) { return __uint_as_float(w & 0xffff0000u); }
; __device__ __forceinline__ float sigmoidf_(float x) { return __builtin_amdgcn_rcpf(1.0f + fexp_(-x)); }
; __device__ __forceinline__ void ret_r3_phase(LAS unsigned char* lds, const bf16_t* proj, const float* cosT, const float* sinT, const float* gst, bf16_t* ycat, int G, int b) {
;     ...
;                 sq += __shfl_xor(sq, 1); sq += __shfl_xor(sq, 2); sq += __shfl_xor(sq, 4);
;                 const float rstd = 1.0f / sqrtf(sq * (1.0f / 128.0f) + GN_EPS);
;                 const unsigned gw[8] = {gc0.x, gc0.y, gc0.z, gc0.w, gc1.x, gc1.y, gc1.z, gc1.w};
;                 if (F8 & 1) {
;                     float y[16];
; #pragma unroll
;                     for (int j = 0; j < 8; ++j) { const float ga = bflo(gw[j]), gb = bfhi(gw[j]); y[2 * j] = ga * sigmoidf_(ga) * v[2 * j] * rstd; y[2 * j + 1] = gb * sigmoidf_(gb) * v[2 * j + 1] * rstd; }
;                     *(u32x4*)((unsigned char*)ycat + (size_t)s * D_ + h * 128 + tq * 16) = (u32x4){pk4_fp8(y[0], y[1], y[2], y[3]), pk4_fp8(y[4], y[5], y[6], y[7]), pk4_fp8(y[8], y[9], y[10], y[11]), pk4_fp8(y[12], y[13], y[14], y[15])};
;                 } else {
;                 unsigned ow[8];
; #pragma unroll
;                 for (int j = 0; j < 8; ++j) { const float ga = bflo(gw[j]), gb = bfhi(gw[j]);
;                     ow[j] = pk2(ga * sigmoidf_(ga) * v[2 * j] * rstd, gb * sigmoidf_(gb) * v[2 * j + 1] * rstd); }
;                 bf16_t* yp = ycat + (size_t)s * D_ + h * 128 + tq * 16;
;                 *(u32x4*)yp = (u32x4){ow[0], ow[1], ow[2], ow[3]}; *(u32x4*)(yp + 8) = (u32x4){ow[4], ow[5], ow[6], ow[7]};
;                 }
;             }
;         }
;         __syncthreads();
	v_add_f32_dpp v6, v6, v6 quad_perm:[1,0,3,2] row_mask:0xf bank_mask:0xf
	s_nop 1
	s_waitcnt lgkmcnt(0)
	v_add_f32_dpp v6, v6, v6 quad_perm:[2,3,0,1] row_mask:0xf bank_mask:0xf
	s_nop 1
	s_waitcnt lgkmcnt(0)
	v_add_f32_dpp v6, v6, v6 row_half_mirror row_mask:0xf bank_mask:0xf
	v_fmamk_f32 v6, v6, 0x3c000000, v185
	v_cmp_gt_f32_e32 vcc, s6, v6
	v_mul_f32_e32 v10, 0x4f800000, v6
	s_nop 0
	v_cndmask_b32_e32 v6, v6, v10, vcc
	v_sqrt_f32_e32 v10, v6
	s_nop 0
	v_add_u32_e32 v14, -1, v10
	v_fma_f32 v15, -v14, v10, v6
	v_cmp_ge_f32_e64 s[0:1], 0, v15
	v_add_u32_e32 v15, 1, v10
	s_nop 0
	v_cndmask_b32_e64 v14, v10, v14, s[0:1]
	v_fma_f32 v10, -v15, v10, v6
	v_cmp_lt_f32_e64 s[0:1], 0, v10
	s_nop 1
	v_cndmask_b32_e64 v10, v14, v15, s[0:1]
	v_mul_f32_e32 v14, 0x37800000, v10
	v_cndmask_b32_e32 v10, v10, v14, vcc
	v_cmp_class_f32_e32 vcc, v6, v186
	s_nop 1
	v_cndmask_b32_e32 v6, v10, v6, vcc
	v_div_scale_f32 v10, s[0:1], v6, v6, 1.0
	v_rcp_f32_e32 v14, v10
	s_nop 0
	v_fma_f32 v15, -v10, v14, 1.0
	v_fmac_f32_e32 v14, v15, v14
	v_div_scale_f32 v15, vcc, 1.0, v6, 1.0
	v_mul_f32_e32 v26, v15, v14
	v_fma_f32 v27, -v10, v26, v15
	v_fmac_f32_e32 v26, v27, v14
	v_fma_f32 v10, -v10, v26, v15
	v_div_fmas_f32 v10, v10, v14, v26
	v_div_fixup_f32 v6, v10, v6, 1.0
	v_lshlrev_b32_e32 v10, 16, v22
	v_mul_f32_e32 v15, 0xbfb8aa3b, v10
	v_exp_f32_e32 v15, v15
	v_and_b32_e32 v14, 0xffff0000, v22
	v_and_b32_e32 v22, 0xffff0000, v25
	v_add_f32_e32 v15, 1.0, v15
	v_rcp_f32_e32 v15, v15
	s_nop 0
	v_mul_f32_e32 v10, v15, v10
	v_mul_f32_e32 v15, 0xbfb8aa3b, v14
	v_exp_f32_e32 v15, v15
	v_mul_f32_e32 v10, v10, v18
	v_and_b32_e32 v18, 0xffff0000, v23
	v_mul_f32_e32 v10, v10, v6
	v_add_f32_e32 v15, 1.0, v15
	v_rcp_f32_e32 v15, v15
	s_nop 0
	v_mul_f32_e32 v14, v15, v14
	v_lshlrev_b32_e32 v15, 16, v23
	v_mul_f32_e32 v14, v14, v19
	v_mul_f32_e32 v19, 0xbfb8aa3b, v15
	v_exp_f32_e32 v19, v19
	v_mul_f32_e32 v14, v14, v6
	v_add_f32_e32 v19, 1.0, v19
	v_rcp_f32_e32 v19, v19
	s_nop 0
	v_mul_f32_e32 v15, v19, v15
	v_mul_f32_e32 v19, 0xbfb8aa3b, v18
	v_exp_f32_e32 v19, v19
	v_mul_f32_e32 v15, v15, v20
	v_and_b32_e32 v20, 0xffff0000, v24
	v_mul_f32_e32 v15, v15, v6
	v_add_f32_e32 v19, 1.0, v19
	v_rcp_f32_e32 v19, v19
	s_nop 0
	v_mul_f32_e32 v18, v19, v18
	v_lshlrev_b32_e32 v19, 16, v24
	v_mul_f32_e32 v18, v18, v21
	v_mul_f32_e32 v21, 0xbfb8aa3b, v19
	v_exp_f32_e32 v21, v21
	v_mul_f32_e32 v18, v18, v6
	v_add_f32_e32 v21, 1.0, v21
	v_rcp_f32_e32 v21, v21
	s_nop 0
	v_mul_f32_e32 v19, v21, v19
	v_mul_f32_e32 v21, 0xbfb8aa3b, v20
	v_exp_f32_e32 v21, v21
	v_mul_f32_e32 v19, v19, v29
	v_mul_f32_e32 v19, v19, v6
	v_add_f32_e32 v21, 1.0, v21
	v_rcp_f32_e32 v21, v21
	s_nop 0
	v_mul_f32_e32 v20, v21, v20
	v_lshlrev_b32_e32 v21, 16, v25
	v_mul_f32_e32 v23, 0xbfb8aa3b, v21
	v_exp_f32_e32 v23, v23
	v_mul_f32_e32 v20, v20, v30
	v_mul_f32_e32 v20, v20, v6
	v_add_f32_e32 v23, 1.0, v23
	v_rcp_f32_e32 v23, v23
	s_nop 0
	v_mul_f32_e32 v21, v23, v21
	v_mul_f32_e32 v16, v21, v16
	v_mul_f32_e32 v21, 0xbfb8aa3b, v22
	v_exp_f32_e32 v21, v21
	v_mul_f32_e32 v16, v16, v6
	v_add_f32_e32 v21, 1.0, v21
	v_rcp_f32_e32 v21, v21
	s_nop 0
	v_mul_f32_e32 v21, v21, v22
	v_mul_f32_e32 v17, v21, v17
	v_lshlrev_b32_e32 v21, 16, v2
	v_mul_f32_e32 v22, 0xbfb8aa3b, v21
	v_exp_f32_e32 v22, v22
	v_and_b32_e32 v2, 0xffff0000, v2
	v_mul_f32_e32 v17, v17, v6
	v_add_f32_e32 v22, 1.0, v22
	v_rcp_f32_e32 v22, v22
	s_nop 0
	v_mul_f32_e32 v21, v22, v21
	v_mul_f32_e32 v22, 0xbfb8aa3b, v2
	v_exp_f32_e32 v22, v22
	v_mul_f32_e32 v21, v21, v31
	v_mul_f32_e32 v21, v21, v6
	v_add_f32_e32 v22, 1.0, v22
	v_rcp_f32_e32 v22, v22
	s_nop 0
	v_mul_f32_e32 v2, v22, v2
	v_mul_f32_e32 v2, v2, v32
	v_mul_f32_e32 v22, v2, v6
	v_lshlrev_b32_e32 v2, 16, v3
	v_mul_f32_e32 v23, 0xbfb8aa3b, v2
	v_exp_f32_e32 v23, v23
	v_and_b32_e32 v3, 0xffff0000, v3
	v_add_f32_e32 v23, 1.0, v23
	v_rcp_f32_e32 v23, v23
	s_nop 0
	v_mul_f32_e32 v2, v23, v2
	v_mul_f32_e32 v2, v2, v12
	v_mul_f32_e32 v12, v2, v6
	v_mul_f32_e32 v2, 0xbfb8aa3b, v3
	v_exp_f32_e32 v2, v2
	s_nop 0
	v_add_f32_e32 v2, 1.0, v2
	v_rcp_f32_e32 v2, v2
	s_nop 0
	v_mul_f32_e32 v2, v2, v3
	v_mul_f32_e32 v2, v2, v13
	v_mul_f32_e32 v13, v2, v6
	v_lshlrev_b32_e32 v2, 16, v4
	v_and_b32_e32 v3, 0xffff0000, v4
	v_mul_f32_e32 v4, 0xbfb8aa3b, v2
	v_exp_f32_e32 v4, v4
	s_nop 0
	v_add_f32_e32 v4, 1.0, v4
	v_rcp_f32_e32 v4, v4
	s_nop 0
	v_mul_f32_e32 v2, v4, v2
	v_mul_f32_e32 v2, v2, v11
	v_mul_f32_e32 v11, v2, v6
	v_mul_f32_e32 v2, 0xbfb8aa3b, v3
	v_exp_f32_e32 v2, v2
	s_nop 0
	v_add_f32_e32 v2, 1.0, v2
	v_rcp_f32_e32 v2, v2
	s_nop 0
	v_mul_f32_e32 v2, v2, v3
	v_mul_f32_e32 v2, v2, v7
	v_mul_f32_e32 v7, v2, v6
	v_lshlrev_b32_e32 v2, 16, v5
	v_mul_f32_e32 v4, 0xbfb8aa3b, v2
	v_exp_f32_e32 v4, v4
	v_and_b32_e32 v3, 0xffff0000, v5
	v_med3_f32 v7, v7, s7, v213
	v_add_f32_e32 v4, 1.0, v4
	v_rcp_f32_e32 v4, v4
	s_nop 0
	v_mul_f32_e32 v2, v4, v2
	v_mul_f32_e32 v2, v2, v8
	v_mul_f32_e32 v5, v2, v6
	v_mul_f32_e32 v2, 0xbfb8aa3b, v3
	v_exp_f32_e32 v2, v2
	v_med3_f32 v4, v14, s7, v213
	v_med3_f32 v8, v15, s7, v213
	v_add_f32_e32 v2, 1.0, v2
	v_rcp_f32_e32 v2, v2
	s_nop 0
	v_mul_f32_e32 v2, v2, v3
	v_mul_f32_e32 v2, v2, v9
	v_mul_f32_e32 v6, v2, v6
	v_med3_f32 v3, v10, s7, v213
	v_mov_b32_e32 v2, v107
	v_cvt_pk_fp8_f32 v2, v3, v4
	v_med3_f32 v9, v18, s7, v213
	v_med3_f32 v4, v19, s7, v213
	v_mov_b32_e32 v3, v107
	v_cvt_pk_fp8_f32 v2, v8, v9 op_sel:[0,0,1]
	v_med3_f32 v8, v20, s7, v213
	v_cvt_pk_fp8_f32 v3, v4, v8
	v_med3_f32 v9, v16, s7, v213
	v_med3_f32 v10, v17, s7, v213
	v_med3_f32 v8, v21, s7, v213
	v_cvt_pk_fp8_f32 v3, v9, v10 op_sel:[0,0,1]
	v_med3_f32 v9, v22, s7, v213
	v_mov_b32_e32 v4, v107
	v_cvt_pk_fp8_f32 v4, v8, v9
	v_med3_f32 v8, v11, s7, v213
	v_med3_f32 v9, v5, s7, v213
	v_mov_b32_e32 v5, v107
	v_cvt_pk_fp8_f32 v5, v8, v7
	v_med3_f32 v10, v12, s7, v213
	v_med3_f32 v12, v13, s7, v213
	v_med3_f32 v6, v6, s7, v213
	v_cvt_pk_fp8_f32 v4, v10, v12 op_sel:[0,0,1]
	v_cvt_pk_fp8_f32 v5, v9, v6 op_sel:[0,0,1]
	v_lshlrev_b64 v[6:7], 11, v[42:43]
	v_lshl_add_u64 v[6:7], v[120:121], 0, v[6:7]
	global_store_dwordx4 v[6:7], v[2:5], off
	s_barrier
	s_cbranch_scc0 .LBB0_404
	v_readlane_b32 s22, v243, 9
	v_readlane_b32 s24, v243, 11
	v_readlane_b32 s26, v243, 13
	v_readlane_b32 s30, v243, 15
	v_readlane_b32 s56, v243, 17
	v_readlane_b32 s12, v243, 25
	v_readlane_b32 s46, v243, 27
	v_readlane_b32 s23, v243, 10
	v_readlane_b32 s25, v243, 12
	v_readlane_b32 s27, v243, 14
	v_readlane_b32 s31, v243, 16
	v_readlane_b32 s57, v243, 18
	v_readlane_b32 s13, v243, 26
	v_readlane_b32 s47, v243, 28
